# p0 adaLN GEMV: weight rows fetched four k-steps ahead (k loop unrolled by four, last four steps peeled)
# baseline (speedup 1.0000x reference)
; __device__ __forceinline__ void p0_prologue(const Frame& F) {
;     ...
;             const int l = it / 96, cb = it % 96, col = cb * 64 + lane;
;             const float* wm = wmod + (size_t)l * D * 6144 + (size_t)(128 * wave) * 6144 + col;
;             float acc[17];
; #pragma unroll
;             for (int r = 0; r < 17; ++r) acc[r] = 0.f;
;             for (int k = 0; k < 128; k += 8) {
;                 float w[8];
; #pragma unroll
;                 for (int q = 0; q < 8; ++q) w[q] = wm[(size_t)(k + q) * 6144];
.LBB0_12:
	s_mul_hi_i32 s4, s30, 0x2aaaaaab
	s_lshr_b32 s5, s4, 31
	s_ashr_i32 s4, s4, 4
	s_add_i32 s9, s4, s5
	s_mul_i32 s4, s9, 0x60
	s_sub_i32 s4, s30, s4
	s_lshl_b32 s8, s4, 6
	s_mul_i32 s4, s9, 0x1800000
	v_add_u32_e32 v6, s8, v38
	s_mul_hi_i32 s5, s9, 0x1800000
	s_add_u32 s4, s17, s4
	v_ashrrev_i32_e32 v7, 31, v6
	s_addc_u32 s5, s18, s5
	v_lshl_add_u64 v[6:7], v[6:7], 2, s[4:5]
	s_mov_b32 s10, -8
	s_mov_b32 s11, s16
	v_mov_b32_e32 v8, 0
	v_mov_b32_e32 v9, v3
	v_mov_b32_e32 v10, 0
	v_mov_b32_e32 v11, v3
	v_mov_b32_e32 v12, 0
	v_mov_b32_e32 v13, v3
	v_mov_b32_e32 v14, 0
	v_mov_b32_e32 v15, v3
	v_mov_b32_e32 v16, 0
	v_mov_b32_e32 v17, v3
	v_mov_b32_e32 v18, 0
	v_mov_b32_e32 v19, v3
	v_mov_b32_e32 v20, 0
	v_mov_b32_e32 v21, v3
	v_mov_b32_e32 v22, 0
	v_mov_b32_e32 v23, v3
	v_mov_b32_e32 v41, 0
	v_add_co_u32_e64 v24, s[4:5], s19, v6
	global_load_dword v182, v[6:7], off
	s_nop 1
	v_addc_co_u32_e64 v25, s[4:5], -1, v7, s[4:5]
	v_add_co_u32_e64 v26, s[4:5], s20, v6
	s_nop 1
	v_addc_co_u32_e64 v27, s[4:5], -1, v7, s[4:5]
	v_add_co_u32_e64 v28, s[4:5], s21, v6
	s_nop 1
	v_addc_co_u32_e64 v29, s[4:5], -1, v7, s[4:5]
	v_add_co_u32_e64 v30, s[4:5], s22, v6
	s_nop 1
	v_addc_co_u32_e64 v31, s[4:5], -1, v7, s[4:5]
	v_add_co_u32_e64 v32, s[4:5], s23, v6
	s_nop 1
	v_addc_co_u32_e64 v33, s[4:5], -1, v7, s[4:5]
	v_add_co_u32_e64 v34, s[4:5], s27, v6
	s_nop 1
	v_addc_co_u32_e64 v35, s[4:5], -1, v7, s[4:5]
	v_add_co_u32_e64 v36, s[4:5], s28, v6
	s_nop 1
	v_addc_co_u32_e64 v37, s[4:5], -1, v7, s[4:5]
	global_load_dword v183, v[24:25], off
	global_load_dword v184, v[26:27], off
	global_load_dword v185, v[28:29], off
	global_load_dword v186, v[30:31], off
	global_load_dword v187, v[32:33], off
	global_load_dword v188, v[34:35], off
	global_load_dword v189, v[36:37], off
	v_lshl_add_u64 v[6:7], v[6:7], 0, s[6:7]
	v_add_co_u32_e64 v24, s[4:5], s19, v6
	global_load_dword v190, v[6:7], off
	s_nop 1
	v_addc_co_u32_e64 v25, s[4:5], -1, v7, s[4:5]
	v_add_co_u32_e64 v26, s[4:5], s20, v6
	s_nop 1
	v_addc_co_u32_e64 v27, s[4:5], -1, v7, s[4:5]
	v_add_co_u32_e64 v28, s[4:5], s21, v6
	s_nop 1
	v_addc_co_u32_e64 v29, s[4:5], -1, v7, s[4:5]
	v_add_co_u32_e64 v30, s[4:5], s22, v6
	s_nop 1
	v_addc_co_u32_e64 v31, s[4:5], -1, v7, s[4:5]
	v_add_co_u32_e64 v32, s[4:5], s23, v6
	s_nop 1
	v_addc_co_u32_e64 v33, s[4:5], -1, v7, s[4:5]
	v_add_co_u32_e64 v34, s[4:5], s27, v6
	s_nop 1
	v_addc_co_u32_e64 v35, s[4:5], -1, v7, s[4:5]
	v_add_co_u32_e64 v36, s[4:5], s28, v6
	s_nop 1
	v_addc_co_u32_e64 v37, s[4:5], -1, v7, s[4:5]
	global_load_dword v191, v[24:25], off
	global_load_dword v192, v[26:27], off
	global_load_dword v193, v[28:29], off
	global_load_dword v194, v[30:31], off
	global_load_dword v195, v[32:33], off
	global_load_dword v196, v[34:35], off
	global_load_dword v197, v[36:37], off
	v_lshl_add_u64 v[6:7], v[6:7], 0, s[6:7]
	v_add_co_u32_e64 v24, s[4:5], s19, v6
	global_load_dword v198, v[6:7], off
	s_nop 1
	v_addc_co_u32_e64 v25, s[4:5], -1, v7, s[4:5]
	v_add_co_u32_e64 v26, s[4:5], s20, v6
	s_nop 1
	v_addc_co_u32_e64 v27, s[4:5], -1, v7, s[4:5]
	v_add_co_u32_e64 v28, s[4:5], s21, v6
	s_nop 1
	v_addc_co_u32_e64 v29, s[4:5], -1, v7, s[4:5]
	v_add_co_u32_e64 v30, s[4:5], s22, v6
	s_nop 1
	v_addc_co_u32_e64 v31, s[4:5], -1, v7, s[4:5]
	v_add_co_u32_e64 v32, s[4:5], s23, v6
	s_nop 1
	v_addc_co_u32_e64 v33, s[4:5], -1, v7, s[4:5]
	v_add_co_u32_e64 v34, s[4:5], s27, v6
	s_nop 1
	v_addc_co_u32_e64 v35, s[4:5], -1, v7, s[4:5]
	v_add_co_u32_e64 v36, s[4:5], s28, v6
	s_nop 1
	v_addc_co_u32_e64 v37, s[4:5], -1, v7, s[4:5]
	global_load_dword v199, v[24:25], off
	global_load_dword v200, v[26:27], off
	global_load_dword v201, v[28:29], off
	global_load_dword v202, v[30:31], off
	global_load_dword v203, v[32:33], off
	global_load_dword v204, v[34:35], off
	global_load_dword v205, v[36:37], off
	v_lshl_add_u64 v[6:7], v[6:7], 0, s[6:7]
	v_add_co_u32_e64 v24, s[4:5], s19, v6
	global_load_dword v206, v[6:7], off
	s_nop 1
	v_addc_co_u32_e64 v25, s[4:5], -1, v7, s[4:5]
	v_add_co_u32_e64 v26, s[4:5], s20, v6
	s_nop 1
	v_addc_co_u32_e64 v27, s[4:5], -1, v7, s[4:5]
	v_add_co_u32_e64 v28, s[4:5], s21, v6
	s_nop 1
	v_addc_co_u32_e64 v29, s[4:5], -1, v7, s[4:5]
	v_add_co_u32_e64 v30, s[4:5], s22, v6
	s_nop 1
	v_addc_co_u32_e64 v31, s[4:5], -1, v7, s[4:5]
	v_add_co_u32_e64 v32, s[4:5], s23, v6
	s_nop 1
	v_addc_co_u32_e64 v33, s[4:5], -1, v7, s[4:5]
	v_add_co_u32_e64 v34, s[4:5], s27, v6
	s_nop 1
	v_addc_co_u32_e64 v35, s[4:5], -1, v7, s[4:5]
	v_add_co_u32_e64 v36, s[4:5], s28, v6
	s_nop 1
	v_addc_co_u32_e64 v37, s[4:5], -1, v7, s[4:5]
	global_load_dword v207, v[24:25], off
	global_load_dword v208, v[26:27], off
	global_load_dword v209, v[28:29], off
	global_load_dword v210, v[30:31], off
	global_load_dword v211, v[32:33], off
	global_load_dword v212, v[34:35], off
	global_load_dword v213, v[36:37], off
	v_lshl_add_u64 v[6:7], v[6:7], 0, s[6:7]
; #define LAS __attribute__((address_space(3)))
; __device__ __forceinline__ void p0_prologue(const Frame& F) {
;     ...
;             for (int k = 0; k < 128; k += 8) {
;                 float w[8];
; #pragma unroll
;                 for (int q = 0; q < 8; ++q) w[q] = wm[(size_t)(k + q) * 6144];
; #pragma unroll
;                 for (int r = 0; r < 17; ++r) { const f32x4 s0 = *(LAS const f32x4*)(S + r * 1024 + 128 * wave + k), s1 = *(LAS const f32x4*)(S + r * 1024 + 128 * wave + k + 4);
;                     acc[r] += s0[0] * w[0] + s0[1] * w[1] + s0[2] * w[2] + s0[3] * w[3] + s1[0] * w[4] + s1[1] * w[5] + s1[2] * w[6] + s1[3] * w[7]; }
.LBB0_13:
	s_waitcnt vmcnt(24)
	v_mov_b32_e32 v2, v182
	v_mov_b32_e32 v168, v183
	v_mov_b32_e32 v170, v184
	v_mov_b32_e32 v172, v185
	v_mov_b32_e32 v174, v186
	v_mov_b32_e32 v176, v187
	v_mov_b32_e32 v178, v188
	v_mov_b32_e32 v180, v189
	v_mov_b32_e32 v42, s11
	s_add_i32 s10, s10, 8
	v_add_co_u32_e64 v24, s[4:5], s19, v6
	global_load_dword v182, v[6:7], off
	s_nop 1
	v_addc_co_u32_e64 v25, s[4:5], -1, v7, s[4:5]
	v_add_co_u32_e64 v26, s[4:5], s20, v6
	s_nop 1
	v_addc_co_u32_e64 v27, s[4:5], -1, v7, s[4:5]
	v_add_co_u32_e64 v28, s[4:5], s21, v6
	s_nop 1
	v_addc_co_u32_e64 v29, s[4:5], -1, v7, s[4:5]
	v_add_co_u32_e64 v30, s[4:5], s22, v6
	s_nop 1
	v_addc_co_u32_e64 v31, s[4:5], -1, v7, s[4:5]
	v_add_co_u32_e64 v32, s[4:5], s23, v6
	s_nop 1
	v_addc_co_u32_e64 v33, s[4:5], -1, v7, s[4:5]
	v_add_co_u32_e64 v34, s[4:5], s27, v6
	s_nop 1
	v_addc_co_u32_e64 v35, s[4:5], -1, v7, s[4:5]
	v_add_co_u32_e64 v36, s[4:5], s28, v6
	s_nop 1
	v_addc_co_u32_e64 v37, s[4:5], -1, v7, s[4:5]
	global_load_dword v183, v[24:25], off
	global_load_dword v184, v[26:27], off
	global_load_dword v185, v[28:29], off
	global_load_dword v186, v[30:31], off
	global_load_dword v187, v[32:33], off
	global_load_dword v188, v[34:35], off
	global_load_dword v189, v[36:37], off
	v_lshl_add_u64 v[6:7], v[6:7], 0, s[6:7]
	ds_read_b128 v[24:27], v42
	ds_read_b128 v[28:31], v42 offset:16
	ds_read_b128 v[32:35], v42 offset:4096
	ds_read_b128 v[44:47], v42 offset:4112
	ds_read_b128 v[48:51], v42 offset:8192
	ds_read_b128 v[52:55], v42 offset:8208
	ds_read_b128 v[56:59], v42 offset:12288
	ds_read_b128 v[60:63], v42 offset:12304
	ds_read_b128 v[64:67], v42 offset:16384
	ds_read_b128 v[68:71], v42 offset:16400
	ds_read_b128 v[72:75], v42 offset:20480
	ds_read_b128 v[76:79], v42 offset:20496
	ds_read_b128 v[80:83], v42 offset:24576
	ds_read_b128 v[84:87], v42 offset:24592
	ds_read_b128 v[88:91], v42 offset:28672
	ds_read_b128 v[92:95], v42 offset:28688
	ds_read_b128 v[96:99], v42 offset:32768
	ds_read_b128 v[100:103], v42 offset:32784
	ds_read_b128 v[104:107], v42 offset:36864
	ds_read_b128 v[108:111], v42 offset:36880
	ds_read_b128 v[112:115], v42 offset:40960
	ds_read_b128 v[116:119], v42 offset:40976
	ds_read_b128 v[120:123], v42 offset:45056
	ds_read_b128 v[124:127], v42 offset:45072
	ds_read_b128 v[128:131], v42 offset:49152
	ds_read_b128 v[132:135], v42 offset:49168
	ds_read_b128 v[136:139], v42 offset:53248
	ds_read_b128 v[140:143], v42 offset:53264
	ds_read_b128 v[144:147], v42 offset:57344
	ds_read_b128 v[148:151], v42 offset:57360
	ds_read_b128 v[152:155], v42 offset:61440
	ds_read_b128 v[156:159], v42 offset:61456
	s_add_i32 s4, s11, 0x10000
	s_add_i32 s5, s11, 0x10010
	v_mov_b32_e32 v36, s4
	v_mov_b32_e32 v37, s5
	ds_read_b128 v[160:163], v36
	ds_read_b128 v[164:167], v37
	s_waitcnt lgkmcnt(14)
	v_mov_b32_e32 v37, v32
	v_mov_b32_e32 v32, v25
	v_mov_b32_e32 v25, v34
	v_mov_b32_e32 v34, v27
	v_mov_b32_e32 v27, v44
	v_mov_b32_e32 v44, v29
	v_mov_b32_e32 v29, v46
	v_mov_b32_e32 v46, v31
	v_mov_b32_e32 v31, v56
	v_mov_b32_e32 v56, v49
	v_mov_b32_e32 v49, v60
	v_mov_b32_e32 v60, v53
	v_mov_b32_e32 v53, v72
	v_mov_b32_e32 v72, v65
	v_mov_b32_e32 v65, v76
	v_mov_b32_e32 v76, v69
	v_mov_b32_e32 v69, v88
	v_mov_b32_e32 v88, v81
	v_mov_b32_e32 v81, v92
	v_mov_b32_e32 v92, v85
	v_mov_b32_e32 v85, v104
	v_mov_b32_e32 v104, v97
	v_mov_b32_e32 v97, v108
	v_mov_b32_e32 v108, v101
	s_waitcnt lgkmcnt(11)
	v_mov_b32_e32 v101, v120
	v_mov_b32_e32 v120, v113
	s_waitcnt lgkmcnt(10)
	v_mov_b32_e32 v113, v124
	v_mov_b32_e32 v124, v117
	s_waitcnt lgkmcnt(7)
	v_mov_b32_e32 v117, v136
	v_mov_b32_e32 v136, v129
	s_waitcnt lgkmcnt(6)
	v_mov_b32_e32 v129, v140
	v_mov_b32_e32 v140, v133
	s_waitcnt lgkmcnt(3)
	v_mov_b32_e32 v133, v152
	v_mov_b32_e32 v152, v145
	v_mov_b32_e32 v36, v24
	v_mov_b32_e32 v24, v26
	v_mov_b32_e32 v26, v28
	v_mov_b32_e32 v28, v30
	v_mov_b32_e32 v30, v48
	v_mov_b32_e32 v48, v52
	v_mov_b32_e32 v52, v64
	v_mov_b32_e32 v64, v68
	v_mov_b32_e32 v68, v80
	v_mov_b32_e32 v80, v84
	v_mov_b32_e32 v84, v96
	v_mov_b32_e32 v96, v100
	v_mov_b32_e32 v100, v112
	v_mov_b32_e32 v112, v116
	v_mov_b32_e32 v116, v128
	v_mov_b32_e32 v128, v132
	v_mov_b32_e32 v132, v144
	v_mov_b32_e32 v144, v148
	s_waitcnt lgkmcnt(2)
	v_mov_b32_e32 v145, v156
	v_mov_b32_e32 v156, v149
	v_mov_b32_e32 v42, v50
	v_mov_b32_e32 v43, v58
	v_mov_b32_e32 v58, v51
	v_mov_b32_e32 v50, v54
	v_mov_b32_e32 v51, v62
	v_mov_b32_e32 v62, v55
	v_mov_b32_e32 v54, v66
	v_mov_b32_e32 v55, v74
	v_mov_b32_e32 v74, v67
	v_mov_b32_e32 v66, v70
	v_mov_b32_e32 v67, v78
	v_mov_b32_e32 v78, v71
	v_mov_b32_e32 v70, v82
	v_mov_b32_e32 v71, v90
	v_pk_mul_f32 v[32:33], v[170:171], v[32:33] op_sel_hi:[0,1]
	v_pk_mul_f32 v[56:57], v[170:171], v[56:57] op_sel_hi:[0,1]
	v_pk_mul_f32 v[72:73], v[170:171], v[72:73] op_sel_hi:[0,1]
	v_pk_mul_f32 v[88:89], v[170:171], v[88:89] op_sel_hi:[0,1]
	v_pk_mul_f32 v[104:105], v[170:171], v[104:105] op_sel_hi:[0,1]
	v_pk_mul_f32 v[120:121], v[170:171], v[120:121] op_sel_hi:[0,1]
	v_pk_mul_f32 v[136:137], v[170:171], v[136:137] op_sel_hi:[0,1]
	v_pk_mul_f32 v[148:149], v[170:171], v[152:153] op_sel_hi:[0,1]
	v_mov_b32_e32 v90, v83
	v_mov_b32_e32 v82, v86
	v_mov_b32_e32 v83, v94
	v_mov_b32_e32 v94, v87
	v_mov_b32_e32 v86, v98
	v_mov_b32_e32 v87, v106
	v_mov_b32_e32 v106, v99
	v_mov_b32_e32 v98, v102
	v_mov_b32_e32 v99, v110
	v_mov_b32_e32 v110, v103
	v_mov_b32_e32 v102, v114
	v_mov_b32_e32 v103, v122
	v_mov_b32_e32 v122, v115
	v_mov_b32_e32 v114, v118
	v_mov_b32_e32 v115, v126
	v_mov_b32_e32 v126, v119
	v_mov_b32_e32 v118, v130
	v_mov_b32_e32 v119, v138
	v_mov_b32_e32 v138, v131
	v_mov_b32_e32 v130, v134
	v_mov_b32_e32 v131, v142
	v_mov_b32_e32 v142, v135
	v_mov_b32_e32 v134, v146
	v_mov_b32_e32 v135, v154
	v_pk_fma_f32 v[32:33], v[168:169], v[36:37], v[32:33] op_sel_hi:[0,1,1]
	v_pk_fma_f32 v[30:31], v[168:169], v[30:31], v[56:57] op_sel_hi:[0,1,1]
	v_pk_fma_f32 v[36:37], v[168:169], v[52:53], v[72:73] op_sel_hi:[0,1,1]
	v_pk_fma_f32 v[52:53], v[168:169], v[68:69], v[88:89] op_sel_hi:[0,1,1]
	v_pk_fma_f32 v[56:57], v[168:169], v[84:85], v[104:105] op_sel_hi:[0,1,1]
	v_pk_fma_f32 v[68:69], v[168:169], v[100:101], v[120:121] op_sel_hi:[0,1,1]
	v_pk_fma_f32 v[72:73], v[168:169], v[116:117], v[136:137] op_sel_hi:[0,1,1]
	v_pk_fma_f32 v[84:85], v[168:169], v[132:133], v[148:149] op_sel_hi:[0,1,1]
	v_mov_b32_e32 v169, v170
	v_mov_b32_e32 v154, v147
	v_pk_fma_f32 v[24:25], v[172:173], v[24:25], v[32:33] op_sel_hi:[0,1,1]
	v_pk_fma_f32 v[30:31], v[172:173], v[42:43], v[30:31] op_sel_hi:[0,1,1]
	v_pk_fma_f32 v[32:33], v[172:173], v[54:55], v[36:37] op_sel_hi:[0,1,1]
	v_pk_fma_f32 v[36:37], v[172:173], v[70:71], v[52:53] op_sel_hi:[0,1,1]
	v_pk_fma_f32 v[42:43], v[172:173], v[86:87], v[56:57] op_sel_hi:[0,1,1]
	v_pk_fma_f32 v[52:53], v[172:173], v[102:103], v[68:69] op_sel_hi:[0,1,1]
	v_pk_fma_f32 v[54:55], v[172:173], v[118:119], v[72:73] op_sel_hi:[0,1,1]
	v_pk_fma_f32 v[56:57], v[172:173], v[134:135], v[84:85] op_sel_hi:[0,1,1]
	s_waitcnt lgkmcnt(1)
; #define LAS __attribute__((address_space(3)))
; __device__ __forceinline__ void p0_prologue(const Frame& F) {
;     ...
;             for (int k = 0; k < 128; k += 8) {
;                 float w[8];
; #pragma unroll
;                 for (int q = 0; q < 8; ++q) w[q] = wm[(size_t)(k + q) * 6144];
; #pragma unroll
;                 for (int r = 0; r < 17; ++r) { const f32x4 s0 = *(LAS const f32x4*)(S + r * 1024 + 128 * wave + k), s1 = *(LAS const f32x4*)(S + r * 1024 + 128 * wave + k + 4);
;                     acc[r] += s0[0] * w[0] + s0[1] * w[1] + s0[2] * w[2] + s0[3] * w[3] + s1[0] * w[4] + s1[1] * w[5] + s1[2] * w[6] + s1[3] * w[7]; }
	v_pk_mul_f32 v[68:69], v[168:169], v[160:161]
	v_mov_b32_e32 v173, v174
	v_pk_fma_f32 v[24:25], v[174:175], v[34:35], v[24:25] op_sel_hi:[0,1,1]
	v_pk_fma_f32 v[30:31], v[174:175], v[58:59], v[30:31] op_sel_hi:[0,1,1]
	v_pk_fma_f32 v[32:33], v[174:175], v[74:75], v[32:33] op_sel_hi:[0,1,1]
	v_pk_fma_f32 v[34:35], v[174:175], v[90:91], v[36:37] op_sel_hi:[0,1,1]
	v_pk_fma_f32 v[36:37], v[174:175], v[106:107], v[42:43] op_sel_hi:[0,1,1]
	v_pk_fma_f32 v[42:43], v[174:175], v[122:123], v[52:53] op_sel_hi:[0,1,1]
	v_pk_fma_f32 v[52:53], v[174:175], v[138:139], v[54:55] op_sel_hi:[0,1,1]
	v_pk_fma_f32 v[54:55], v[174:175], v[154:155], v[56:57] op_sel_hi:[0,1,1]
	v_pk_mul_f32 v[56:57], v[172:173], v[162:163]
	v_add_f32_e32 v58, v68, v69
	v_pk_fma_f32 v[24:25], v[176:177], v[26:27], v[24:25] op_sel_hi:[0,1,1]
	v_pk_fma_f32 v[26:27], v[176:177], v[48:49], v[30:31] op_sel_hi:[0,1,1]
	v_pk_fma_f32 v[30:31], v[176:177], v[64:65], v[32:33] op_sel_hi:[0,1,1]
	v_pk_fma_f32 v[32:33], v[176:177], v[80:81], v[34:35] op_sel_hi:[0,1,1]
	v_pk_fma_f32 v[34:35], v[176:177], v[96:97], v[36:37] op_sel_hi:[0,1,1]
	v_pk_fma_f32 v[36:37], v[176:177], v[112:113], v[42:43] op_sel_hi:[0,1,1]
	v_pk_fma_f32 v[42:43], v[176:177], v[128:129], v[52:53] op_sel_hi:[0,1,1]
	v_pk_fma_f32 v[48:49], v[176:177], v[144:145], v[54:55] op_sel_hi:[0,1,1]
	v_mov_b32_e32 v177, v178
	v_add_f32_e32 v52, v56, v58
	v_mov_b32_e32 v146, v150
	v_mov_b32_e32 v147, v158
	v_pk_fma_f32 v[24:25], v[178:179], v[44:45], v[24:25] op_sel_hi:[0,1,1]
	v_pk_fma_f32 v[26:27], v[178:179], v[60:61], v[26:27] op_sel_hi:[0,1,1]
	v_pk_fma_f32 v[30:31], v[178:179], v[76:77], v[30:31] op_sel_hi:[0,1,1]
	v_pk_fma_f32 v[32:33], v[178:179], v[92:93], v[32:33] op_sel_hi:[0,1,1]
	v_pk_fma_f32 v[34:35], v[178:179], v[108:109], v[34:35] op_sel_hi:[0,1,1]
	v_pk_fma_f32 v[36:37], v[178:179], v[124:125], v[36:37] op_sel_hi:[0,1,1]
	v_pk_fma_f32 v[42:43], v[178:179], v[140:141], v[42:43] op_sel_hi:[0,1,1]
	v_pk_fma_f32 v[44:45], v[178:179], v[156:157], v[48:49] op_sel_hi:[0,1,1]
	s_waitcnt lgkmcnt(0)
	v_pk_mul_f32 v[48:49], v[176:177], v[164:165]
	v_add_f32_e32 v52, v57, v52
	v_mov_b32_e32 v158, v151
	v_pk_fma_f32 v[24:25], v[180:181], v[28:29], v[24:25] op_sel_hi:[0,1,1]
	v_pk_fma_f32 v[26:27], v[180:181], v[50:51], v[26:27] op_sel_hi:[0,1,1]
	v_pk_fma_f32 v[28:29], v[180:181], v[66:67], v[30:31] op_sel_hi:[0,1,1]
	v_pk_fma_f32 v[30:31], v[180:181], v[82:83], v[32:33] op_sel_hi:[0,1,1]
	v_pk_fma_f32 v[32:33], v[180:181], v[98:99], v[34:35] op_sel_hi:[0,1,1]
	v_pk_fma_f32 v[34:35], v[180:181], v[114:115], v[36:37] op_sel_hi:[0,1,1]
	v_pk_fma_f32 v[36:37], v[180:181], v[130:131], v[42:43] op_sel_hi:[0,1,1]
	v_pk_fma_f32 v[42:43], v[180:181], v[146:147], v[44:45] op_sel_hi:[0,1,1]
	v_mov_b32_e32 v181, v2
	v_add_f32_e32 v48, v48, v52
	v_pk_fma_f32 v[24:25], v[2:3], v[46:47], v[24:25] op_sel_hi:[0,1,1]
	v_pk_fma_f32 v[26:27], v[2:3], v[62:63], v[26:27] op_sel_hi:[0,1,1]
	v_pk_fma_f32 v[28:29], v[2:3], v[78:79], v[28:29] op_sel_hi:[0,1,1]
	v_pk_fma_f32 v[30:31], v[2:3], v[94:95], v[30:31] op_sel_hi:[0,1,1]
	v_pk_fma_f32 v[32:33], v[2:3], v[110:111], v[32:33] op_sel_hi:[0,1,1]
	v_pk_fma_f32 v[34:35], v[2:3], v[126:127], v[34:35] op_sel_hi:[0,1,1]
	v_pk_fma_f32 v[36:37], v[2:3], v[142:143], v[36:37] op_sel_hi:[0,1,1]
	v_pk_fma_f32 v[42:43], v[2:3], v[158:159], v[42:43] op_sel_hi:[0,1,1]
	v_pk_mul_f32 v[44:45], v[180:181], v[166:167]
	v_add_f32_e32 v2, v49, v48
	v_add_f32_e32 v2, v44, v2
	s_add_i32 s11, s11, 32
	v_add_f32_e32 v2, v45, v2
	v_pk_add_f32 v[8:9], v[8:9], v[24:25]
	v_pk_add_f32 v[10:11], v[10:11], v[26:27]
	v_pk_add_f32 v[12:13], v[12:13], v[28:29]
	v_pk_add_f32 v[14:15], v[14:15], v[30:31]
	v_pk_add_f32 v[16:17], v[16:17], v[32:33]
	v_pk_add_f32 v[18:19], v[18:19], v[34:35]
	v_pk_add_f32 v[20:21], v[20:21], v[36:37]
	v_pk_add_f32 v[22:23], v[22:23], v[42:43]
	v_add_f32_e32 v41, v41, v2
	s_waitcnt vmcnt(24)
	v_mov_b32_e32 v2, v190
	v_mov_b32_e32 v168, v191
	v_mov_b32_e32 v170, v192
	v_mov_b32_e32 v172, v193
	v_mov_b32_e32 v174, v194
	v_mov_b32_e32 v176, v195
	v_mov_b32_e32 v178, v196
	v_mov_b32_e32 v180, v197
	v_mov_b32_e32 v42, s11
	s_add_i32 s10, s10, 8
	v_add_co_u32_e64 v24, s[4:5], s19, v6
	global_load_dword v190, v[6:7], off
	s_nop 1
	v_addc_co_u32_e64 v25, s[4:5], -1, v7, s[4:5]
	v_add_co_u32_e64 v26, s[4:5], s20, v6
	s_nop 1
	v_addc_co_u32_e64 v27, s[4:5], -1, v7, s[4:5]
	v_add_co_u32_e64 v28, s[4:5], s21, v6
	s_nop 1
	v_addc_co_u32_e64 v29, s[4:5], -1, v7, s[4:5]
	v_add_co_u32_e64 v30, s[4:5], s22, v6
	s_nop 1
	v_addc_co_u32_e64 v31, s[4:5], -1, v7, s[4:5]
	v_add_co_u32_e64 v32, s[4:5], s23, v6
	s_nop 1
	v_addc_co_u32_e64 v33, s[4:5], -1, v7, s[4:5]
	v_add_co_u32_e64 v34, s[4:5], s27, v6
	s_nop 1
	v_addc_co_u32_e64 v35, s[4:5], -1, v7, s[4:5]
	v_add_co_u32_e64 v36, s[4:5], s28, v6
	s_nop 1
	v_addc_co_u32_e64 v37, s[4:5], -1, v7, s[4:5]
	global_load_dword v191, v[24:25], off
	global_load_dword v192, v[26:27], off
	global_load_dword v193, v[28:29], off
	global_load_dword v194, v[30:31], off
	global_load_dword v195, v[32:33], off
	global_load_dword v196, v[34:35], off
	global_load_dword v197, v[36:37], off
	v_lshl_add_u64 v[6:7], v[6:7], 0, s[6:7]
	ds_read_b128 v[24:27], v42
	ds_read_b128 v[28:31], v42 offset:16
	ds_read_b128 v[32:35], v42 offset:4096
	ds_read_b128 v[44:47], v42 offset:4112
	ds_read_b128 v[48:51], v42 offset:8192
	ds_read_b128 v[52:55], v42 offset:8208
	ds_read_b128 v[56:59], v42 offset:12288
	ds_read_b128 v[60:63], v42 offset:12304
	ds_read_b128 v[64:67], v42 offset:16384
	ds_read_b128 v[68:71], v42 offset:16400
	ds_read_b128 v[72:75], v42 offset:20480
	ds_read_b128 v[76:79], v42 offset:20496
	ds_read_b128 v[80:83], v42 offset:24576
	ds_read_b128 v[84:87], v42 offset:24592
	ds_read_b128 v[88:91], v42 offset:28672
	ds_read_b128 v[92:95], v42 offset:28688
	ds_read_b128 v[96:99], v42 offset:32768
	ds_read_b128 v[100:103], v42 offset:32784
	ds_read_b128 v[104:107], v42 offset:36864
	ds_read_b128 v[108:111], v42 offset:36880
	ds_read_b128 v[112:115], v42 offset:40960
	ds_read_b128 v[116:119], v42 offset:40976
	ds_read_b128 v[120:123], v42 offset:45056
	ds_read_b128 v[124:127], v42 offset:45072
	ds_read_b128 v[128:131], v42 offset:49152
	ds_read_b128 v[132:135], v42 offset:49168
	ds_read_b128 v[136:139], v42 offset:53248
	ds_read_b128 v[140:143], v42 offset:53264
	ds_read_b128 v[144:147], v42 offset:57344
	ds_read_b128 v[148:151], v42 offset:57360
	ds_read_b128 v[152:155], v42 offset:61440
	ds_read_b128 v[156:159], v42 offset:61456
	s_add_i32 s4, s11, 0x10000
	s_add_i32 s5, s11, 0x10010
	v_mov_b32_e32 v36, s4
	v_mov_b32_e32 v37, s5
	ds_read_b128 v[160:163], v36
	ds_read_b128 v[164:167], v37
	s_waitcnt lgkmcnt(14)
; #define LAS __attribute__((address_space(3)))
; __device__ __forceinline__ void p0_prologue(const Frame& F) {
;     ...
;             for (int k = 0; k < 128; k += 8) {
;                 float w[8];
; #pragma unroll
;                 for (int q = 0; q < 8; ++q) w[q] = wm[(size_t)(k + q) * 6144];
; #pragma unroll
;                 for (int r = 0; r < 17; ++r) { const f32x4 s0 = *(LAS const f32x4*)(S + r * 1024 + 128 * wave + k), s1 = *(LAS const f32x4*)(S + r * 1024 + 128 * wave + k + 4);
;                     acc[r] += s0[0] * w[0] + s0[1] * w[1] + s0[2] * w[2] + s0[3] * w[3] + s1[0] * w[4] + s1[1] * w[5] + s1[2] * w[6] + s1[3] * w[7]; }
	v_mov_b32_e32 v37, v32
	v_mov_b32_e32 v32, v25
	v_mov_b32_e32 v25, v34
	v_mov_b32_e32 v34, v27
	v_mov_b32_e32 v27, v44
	v_mov_b32_e32 v44, v29
	v_mov_b32_e32 v29, v46
	v_mov_b32_e32 v46, v31
	v_mov_b32_e32 v31, v56
	v_mov_b32_e32 v56, v49
	v_mov_b32_e32 v49, v60
	v_mov_b32_e32 v60, v53
	v_mov_b32_e32 v53, v72
	v_mov_b32_e32 v72, v65
	v_mov_b32_e32 v65, v76
	v_mov_b32_e32 v76, v69
	v_mov_b32_e32 v69, v88
	v_mov_b32_e32 v88, v81
	v_mov_b32_e32 v81, v92
	v_mov_b32_e32 v92, v85
	v_mov_b32_e32 v85, v104
	v_mov_b32_e32 v104, v97
	v_mov_b32_e32 v97, v108
	v_mov_b32_e32 v108, v101
	s_waitcnt lgkmcnt(11)
	v_mov_b32_e32 v101, v120
	v_mov_b32_e32 v120, v113
	s_waitcnt lgkmcnt(10)
	v_mov_b32_e32 v113, v124
	v_mov_b32_e32 v124, v117
	s_waitcnt lgkmcnt(7)
	v_mov_b32_e32 v117, v136
	v_mov_b32_e32 v136, v129
	s_waitcnt lgkmcnt(6)
	v_mov_b32_e32 v129, v140
	v_mov_b32_e32 v140, v133
	s_waitcnt lgkmcnt(3)
	v_mov_b32_e32 v133, v152
	v_mov_b32_e32 v152, v145
	v_mov_b32_e32 v36, v24
	v_mov_b32_e32 v24, v26
	v_mov_b32_e32 v26, v28
	v_mov_b32_e32 v28, v30
	v_mov_b32_e32 v30, v48
	v_mov_b32_e32 v48, v52
	v_mov_b32_e32 v52, v64
	v_mov_b32_e32 v64, v68
	v_mov_b32_e32 v68, v80
	v_mov_b32_e32 v80, v84
	v_mov_b32_e32 v84, v96
	v_mov_b32_e32 v96, v100
	v_mov_b32_e32 v100, v112
	v_mov_b32_e32 v112, v116
	v_mov_b32_e32 v116, v128
	v_mov_b32_e32 v128, v132
	v_mov_b32_e32 v132, v144
	v_mov_b32_e32 v144, v148
	s_waitcnt lgkmcnt(2)
	v_mov_b32_e32 v145, v156
	v_mov_b32_e32 v156, v149
	v_mov_b32_e32 v42, v50
	v_mov_b32_e32 v43, v58
	v_mov_b32_e32 v58, v51
	v_mov_b32_e32 v50, v54
	v_mov_b32_e32 v51, v62
	v_mov_b32_e32 v62, v55
	v_mov_b32_e32 v54, v66
	v_mov_b32_e32 v55, v74
	v_mov_b32_e32 v74, v67
	v_mov_b32_e32 v66, v70
	v_mov_b32_e32 v67, v78
	v_mov_b32_e32 v78, v71
	v_mov_b32_e32 v70, v82
	v_mov_b32_e32 v71, v90
	v_pk_mul_f32 v[32:33], v[170:171], v[32:33] op_sel_hi:[0,1]
	v_pk_mul_f32 v[56:57], v[170:171], v[56:57] op_sel_hi:[0,1]
	v_pk_mul_f32 v[72:73], v[170:171], v[72:73] op_sel_hi:[0,1]
	v_pk_mul_f32 v[88:89], v[170:171], v[88:89] op_sel_hi:[0,1]
	v_pk_mul_f32 v[104:105], v[170:171], v[104:105] op_sel_hi:[0,1]
	v_pk_mul_f32 v[120:121], v[170:171], v[120:121] op_sel_hi:[0,1]
	v_pk_mul_f32 v[136:137], v[170:171], v[136:137] op_sel_hi:[0,1]
	v_pk_mul_f32 v[148:149], v[170:171], v[152:153] op_sel_hi:[0,1]
	v_mov_b32_e32 v90, v83
	v_mov_b32_e32 v82, v86
	v_mov_b32_e32 v83, v94
	v_mov_b32_e32 v94, v87
	v_mov_b32_e32 v86, v98
	v_mov_b32_e32 v87, v106
	v_mov_b32_e32 v106, v99
	v_mov_b32_e32 v98, v102
	v_mov_b32_e32 v99, v110
	v_mov_b32_e32 v110, v103
	v_mov_b32_e32 v102, v114
	v_mov_b32_e32 v103, v122
	v_mov_b32_e32 v122, v115
	v_mov_b32_e32 v114, v118
	v_mov_b32_e32 v115, v126
	v_mov_b32_e32 v126, v119
	v_mov_b32_e32 v118, v130
	v_mov_b32_e32 v119, v138
	v_mov_b32_e32 v138, v131
	v_mov_b32_e32 v130, v134
	v_mov_b32_e32 v131, v142
	v_mov_b32_e32 v142, v135
	v_mov_b32_e32 v134, v146
	v_mov_b32_e32 v135, v154
	v_pk_fma_f32 v[32:33], v[168:169], v[36:37], v[32:33] op_sel_hi:[0,1,1]
	v_pk_fma_f32 v[30:31], v[168:169], v[30:31], v[56:57] op_sel_hi:[0,1,1]
	v_pk_fma_f32 v[36:37], v[168:169], v[52:53], v[72:73] op_sel_hi:[0,1,1]
	v_pk_fma_f32 v[52:53], v[168:169], v[68:69], v[88:89] op_sel_hi:[0,1,1]
	v_pk_fma_f32 v[56:57], v[168:169], v[84:85], v[104:105] op_sel_hi:[0,1,1]
	v_pk_fma_f32 v[68:69], v[168:169], v[100:101], v[120:121] op_sel_hi:[0,1,1]
	v_pk_fma_f32 v[72:73], v[168:169], v[116:117], v[136:137] op_sel_hi:[0,1,1]
	v_pk_fma_f32 v[84:85], v[168:169], v[132:133], v[148:149] op_sel_hi:[0,1,1]
	v_mov_b32_e32 v169, v170
	v_mov_b32_e32 v154, v147
	v_pk_fma_f32 v[24:25], v[172:173], v[24:25], v[32:33] op_sel_hi:[0,1,1]
	v_pk_fma_f32 v[30:31], v[172:173], v[42:43], v[30:31] op_sel_hi:[0,1,1]
	v_pk_fma_f32 v[32:33], v[172:173], v[54:55], v[36:37] op_sel_hi:[0,1,1]
	v_pk_fma_f32 v[36:37], v[172:173], v[70:71], v[52:53] op_sel_hi:[0,1,1]
	v_pk_fma_f32 v[42:43], v[172:173], v[86:87], v[56:57] op_sel_hi:[0,1,1]
	v_pk_fma_f32 v[52:53], v[172:173], v[102:103], v[68:69] op_sel_hi:[0,1,1]
	v_pk_fma_f32 v[54:55], v[172:173], v[118:119], v[72:73] op_sel_hi:[0,1,1]
	v_pk_fma_f32 v[56:57], v[172:173], v[134:135], v[84:85] op_sel_hi:[0,1,1]
	s_waitcnt lgkmcnt(1)
	v_pk_mul_f32 v[68:69], v[168:169], v[160:161]
	v_mov_b32_e32 v173, v174
	v_pk_fma_f32 v[24:25], v[174:175], v[34:35], v[24:25] op_sel_hi:[0,1,1]
	v_pk_fma_f32 v[30:31], v[174:175], v[58:59], v[30:31] op_sel_hi:[0,1,1]
	v_pk_fma_f32 v[32:33], v[174:175], v[74:75], v[32:33] op_sel_hi:[0,1,1]
	v_pk_fma_f32 v[34:35], v[174:175], v[90:91], v[36:37] op_sel_hi:[0,1,1]
	v_pk_fma_f32 v[36:37], v[174:175], v[106:107], v[42:43] op_sel_hi:[0,1,1]
	v_pk_fma_f32 v[42:43], v[174:175], v[122:123], v[52:53] op_sel_hi:[0,1,1]
	v_pk_fma_f32 v[52:53], v[174:175], v[138:139], v[54:55] op_sel_hi:[0,1,1]
	v_pk_fma_f32 v[54:55], v[174:175], v[154:155], v[56:57] op_sel_hi:[0,1,1]
	v_pk_mul_f32 v[56:57], v[172:173], v[162:163]
	v_add_f32_e32 v58, v68, v69
	v_pk_fma_f32 v[24:25], v[176:177], v[26:27], v[24:25] op_sel_hi:[0,1,1]
	v_pk_fma_f32 v[26:27], v[176:177], v[48:49], v[30:31] op_sel_hi:[0,1,1]
	v_pk_fma_f32 v[30:31], v[176:177], v[64:65], v[32:33] op_sel_hi:[0,1,1]
	v_pk_fma_f32 v[32:33], v[176:177], v[80:81], v[34:35] op_sel_hi:[0,1,1]
	v_pk_fma_f32 v[34:35], v[176:177], v[96:97], v[36:37] op_sel_hi:[0,1,1]
	v_pk_fma_f32 v[36:37], v[176:177], v[112:113], v[42:43] op_sel_hi:[0,1,1]
	v_pk_fma_f32 v[42:43], v[176:177], v[128:129], v[52:53] op_sel_hi:[0,1,1]
	v_pk_fma_f32 v[48:49], v[176:177], v[144:145], v[54:55] op_sel_hi:[0,1,1]
	v_mov_b32_e32 v177, v178
	v_add_f32_e32 v52, v56, v58
	v_mov_b32_e32 v146, v150
	v_mov_b32_e32 v147, v158
	v_pk_fma_f32 v[24:25], v[178:179], v[44:45], v[24:25] op_sel_hi:[0,1,1]
	v_pk_fma_f32 v[26:27], v[178:179], v[60:61], v[26:27] op_sel_hi:[0,1,1]
	v_pk_fma_f32 v[30:31], v[178:179], v[76:77], v[30:31] op_sel_hi:[0,1,1]
	v_pk_fma_f32 v[32:33], v[178:179], v[92:93], v[32:33] op_sel_hi:[0,1,1]
	v_pk_fma_f32 v[34:35], v[178:179], v[108:109], v[34:35] op_sel_hi:[0,1,1]
	v_pk_fma_f32 v[36:37], v[178:179], v[124:125], v[36:37] op_sel_hi:[0,1,1]
	v_pk_fma_f32 v[42:43], v[178:179], v[140:141], v[42:43] op_sel_hi:[0,1,1]
	v_pk_fma_f32 v[44:45], v[178:179], v[156:157], v[48:49] op_sel_hi:[0,1,1]
	s_waitcnt lgkmcnt(0)
; #define LAS __attribute__((address_space(3)))
; __device__ __forceinline__ void p0_prologue(const Frame& F) {
;     ...
;             for (int k = 0; k < 128; k += 8) {
;                 float w[8];
; #pragma unroll
;                 for (int q = 0; q < 8; ++q) w[q] = wm[(size_t)(k + q) * 6144];
; #pragma unroll
;                 for (int r = 0; r < 17; ++r) { const f32x4 s0 = *(LAS const f32x4*)(S + r * 1024 + 128 * wave + k), s1 = *(LAS const f32x4*)(S + r * 1024 + 128 * wave + k + 4);
;                     acc[r] += s0[0] * w[0] + s0[1] * w[1] + s0[2] * w[2] + s0[3] * w[3] + s1[0] * w[4] + s1[1] * w[5] + s1[2] * w[6] + s1[3] * w[7]; }
	v_pk_mul_f32 v[48:49], v[176:177], v[164:165]
	v_add_f32_e32 v52, v57, v52
	v_mov_b32_e32 v158, v151
	v_pk_fma_f32 v[24:25], v[180:181], v[28:29], v[24:25] op_sel_hi:[0,1,1]
	v_pk_fma_f32 v[26:27], v[180:181], v[50:51], v[26:27] op_sel_hi:[0,1,1]
	v_pk_fma_f32 v[28:29], v[180:181], v[66:67], v[30:31] op_sel_hi:[0,1,1]
	v_pk_fma_f32 v[30:31], v[180:181], v[82:83], v[32:33] op_sel_hi:[0,1,1]
	v_pk_fma_f32 v[32:33], v[180:181], v[98:99], v[34:35] op_sel_hi:[0,1,1]
	v_pk_fma_f32 v[34:35], v[180:181], v[114:115], v[36:37] op_sel_hi:[0,1,1]
	v_pk_fma_f32 v[36:37], v[180:181], v[130:131], v[42:43] op_sel_hi:[0,1,1]
	v_pk_fma_f32 v[42:43], v[180:181], v[146:147], v[44:45] op_sel_hi:[0,1,1]
	v_mov_b32_e32 v181, v2
	v_add_f32_e32 v48, v48, v52
	v_pk_fma_f32 v[24:25], v[2:3], v[46:47], v[24:25] op_sel_hi:[0,1,1]
	v_pk_fma_f32 v[26:27], v[2:3], v[62:63], v[26:27] op_sel_hi:[0,1,1]
	v_pk_fma_f32 v[28:29], v[2:3], v[78:79], v[28:29] op_sel_hi:[0,1,1]
	v_pk_fma_f32 v[30:31], v[2:3], v[94:95], v[30:31] op_sel_hi:[0,1,1]
	v_pk_fma_f32 v[32:33], v[2:3], v[110:111], v[32:33] op_sel_hi:[0,1,1]
	v_pk_fma_f32 v[34:35], v[2:3], v[126:127], v[34:35] op_sel_hi:[0,1,1]
	v_pk_fma_f32 v[36:37], v[2:3], v[142:143], v[36:37] op_sel_hi:[0,1,1]
	v_pk_fma_f32 v[42:43], v[2:3], v[158:159], v[42:43] op_sel_hi:[0,1,1]
	v_pk_mul_f32 v[44:45], v[180:181], v[166:167]
	v_add_f32_e32 v2, v49, v48
	v_add_f32_e32 v2, v44, v2
	s_add_i32 s11, s11, 32
	v_add_f32_e32 v2, v45, v2
	v_pk_add_f32 v[8:9], v[8:9], v[24:25]
	v_pk_add_f32 v[10:11], v[10:11], v[26:27]
	v_pk_add_f32 v[12:13], v[12:13], v[28:29]
	v_pk_add_f32 v[14:15], v[14:15], v[30:31]
	v_pk_add_f32 v[16:17], v[16:17], v[32:33]
	v_pk_add_f32 v[18:19], v[18:19], v[34:35]
	v_pk_add_f32 v[20:21], v[20:21], v[36:37]
	v_pk_add_f32 v[22:23], v[22:23], v[42:43]
	v_add_f32_e32 v41, v41, v2
	s_waitcnt vmcnt(24)
	v_mov_b32_e32 v2, v198
	v_mov_b32_e32 v168, v199
	v_mov_b32_e32 v170, v200
	v_mov_b32_e32 v172, v201
	v_mov_b32_e32 v174, v202
	v_mov_b32_e32 v176, v203
	v_mov_b32_e32 v178, v204
	v_mov_b32_e32 v180, v205
	v_mov_b32_e32 v42, s11
	s_add_i32 s10, s10, 8
	v_add_co_u32_e64 v24, s[4:5], s19, v6
	global_load_dword v198, v[6:7], off
	s_nop 1
	v_addc_co_u32_e64 v25, s[4:5], -1, v7, s[4:5]
	v_add_co_u32_e64 v26, s[4:5], s20, v6
	s_nop 1
	v_addc_co_u32_e64 v27, s[4:5], -1, v7, s[4:5]
	v_add_co_u32_e64 v28, s[4:5], s21, v6
	s_nop 1
	v_addc_co_u32_e64 v29, s[4:5], -1, v7, s[4:5]
	v_add_co_u32_e64 v30, s[4:5], s22, v6
	s_nop 1
	v_addc_co_u32_e64 v31, s[4:5], -1, v7, s[4:5]
	v_add_co_u32_e64 v32, s[4:5], s23, v6
	s_nop 1
	v_addc_co_u32_e64 v33, s[4:5], -1, v7, s[4:5]
	v_add_co_u32_e64 v34, s[4:5], s27, v6
	s_nop 1
	v_addc_co_u32_e64 v35, s[4:5], -1, v7, s[4:5]
	v_add_co_u32_e64 v36, s[4:5], s28, v6
	s_nop 1
	v_addc_co_u32_e64 v37, s[4:5], -1, v7, s[4:5]
	global_load_dword v199, v[24:25], off
	global_load_dword v200, v[26:27], off
	global_load_dword v201, v[28:29], off
	global_load_dword v202, v[30:31], off
	global_load_dword v203, v[32:33], off
	global_load_dword v204, v[34:35], off
	global_load_dword v205, v[36:37], off
	v_lshl_add_u64 v[6:7], v[6:7], 0, s[6:7]
	ds_read_b128 v[24:27], v42
	ds_read_b128 v[28:31], v42 offset:16
	ds_read_b128 v[32:35], v42 offset:4096
	ds_read_b128 v[44:47], v42 offset:4112
	ds_read_b128 v[48:51], v42 offset:8192
	ds_read_b128 v[52:55], v42 offset:8208
	ds_read_b128 v[56:59], v42 offset:12288
	ds_read_b128 v[60:63], v42 offset:12304
	ds_read_b128 v[64:67], v42 offset:16384
	ds_read_b128 v[68:71], v42 offset:16400
	ds_read_b128 v[72:75], v42 offset:20480
	ds_read_b128 v[76:79], v42 offset:20496
	ds_read_b128 v[80:83], v42 offset:24576
	ds_read_b128 v[84:87], v42 offset:24592
	ds_read_b128 v[88:91], v42 offset:28672
	ds_read_b128 v[92:95], v42 offset:28688
	ds_read_b128 v[96:99], v42 offset:32768
	ds_read_b128 v[100:103], v42 offset:32784
	ds_read_b128 v[104:107], v42 offset:36864
	ds_read_b128 v[108:111], v42 offset:36880
	ds_read_b128 v[112:115], v42 offset:40960
	ds_read_b128 v[116:119], v42 offset:40976
	ds_read_b128 v[120:123], v42 offset:45056
	ds_read_b128 v[124:127], v42 offset:45072
	ds_read_b128 v[128:131], v42 offset:49152
	ds_read_b128 v[132:135], v42 offset:49168
	ds_read_b128 v[136:139], v42 offset:53248
	ds_read_b128 v[140:143], v42 offset:53264
	ds_read_b128 v[144:147], v42 offset:57344
	ds_read_b128 v[148:151], v42 offset:57360
	ds_read_b128 v[152:155], v42 offset:61440
	ds_read_b128 v[156:159], v42 offset:61456
	s_add_i32 s4, s11, 0x10000
	s_add_i32 s5, s11, 0x10010
	v_mov_b32_e32 v36, s4
	v_mov_b32_e32 v37, s5
	ds_read_b128 v[160:163], v36
	ds_read_b128 v[164:167], v37
	s_waitcnt lgkmcnt(14)
	v_mov_b32_e32 v37, v32
	v_mov_b32_e32 v32, v25
	v_mov_b32_e32 v25, v34
	v_mov_b32_e32 v34, v27
	v_mov_b32_e32 v27, v44
	v_mov_b32_e32 v44, v29
	v_mov_b32_e32 v29, v46
	v_mov_b32_e32 v46, v31
	v_mov_b32_e32 v31, v56
	v_mov_b32_e32 v56, v49
	v_mov_b32_e32 v49, v60
	v_mov_b32_e32 v60, v53
	v_mov_b32_e32 v53, v72
	v_mov_b32_e32 v72, v65
	v_mov_b32_e32 v65, v76
	v_mov_b32_e32 v76, v69
	v_mov_b32_e32 v69, v88
	v_mov_b32_e32 v88, v81
	v_mov_b32_e32 v81, v92
	v_mov_b32_e32 v92, v85
	v_mov_b32_e32 v85, v104
	v_mov_b32_e32 v104, v97
	v_mov_b32_e32 v97, v108
	v_mov_b32_e32 v108, v101
	s_waitcnt lgkmcnt(11)
	v_mov_b32_e32 v101, v120
	v_mov_b32_e32 v120, v113
	s_waitcnt lgkmcnt(10)
	v_mov_b32_e32 v113, v124
	v_mov_b32_e32 v124, v117
	s_waitcnt lgkmcnt(7)
	v_mov_b32_e32 v117, v136
	v_mov_b32_e32 v136, v129
	s_waitcnt lgkmcnt(6)
	v_mov_b32_e32 v129, v140
	v_mov_b32_e32 v140, v133
	s_waitcnt lgkmcnt(3)
; #define LAS __attribute__((address_space(3)))
; __device__ __forceinline__ void p0_prologue(const Frame& F) {
;     ...
;             for (int k = 0; k < 128; k += 8) {
;                 float w[8];
; #pragma unroll
;                 for (int q = 0; q < 8; ++q) w[q] = wm[(size_t)(k + q) * 6144];
; #pragma unroll
;                 for (int r = 0; r < 17; ++r) { const f32x4 s0 = *(LAS const f32x4*)(S + r * 1024 + 128 * wave + k), s1 = *(LAS const f32x4*)(S + r * 1024 + 128 * wave + k + 4);
;                     acc[r] += s0[0] * w[0] + s0[1] * w[1] + s0[2] * w[2] + s0[3] * w[3] + s1[0] * w[4] + s1[1] * w[5] + s1[2] * w[6] + s1[3] * w[7]; }
	v_mov_b32_e32 v133, v152
	v_mov_b32_e32 v152, v145
	v_mov_b32_e32 v36, v24
	v_mov_b32_e32 v24, v26
	v_mov_b32_e32 v26, v28
	v_mov_b32_e32 v28, v30
	v_mov_b32_e32 v30, v48
	v_mov_b32_e32 v48, v52
	v_mov_b32_e32 v52, v64
	v_mov_b32_e32 v64, v68
	v_mov_b32_e32 v68, v80
	v_mov_b32_e32 v80, v84
	v_mov_b32_e32 v84, v96
	v_mov_b32_e32 v96, v100
	v_mov_b32_e32 v100, v112
	v_mov_b32_e32 v112, v116
	v_mov_b32_e32 v116, v128
	v_mov_b32_e32 v128, v132
	v_mov_b32_e32 v132, v144
	v_mov_b32_e32 v144, v148
	s_waitcnt lgkmcnt(2)
	v_mov_b32_e32 v145, v156
	v_mov_b32_e32 v156, v149
	v_mov_b32_e32 v42, v50
	v_mov_b32_e32 v43, v58
	v_mov_b32_e32 v58, v51
	v_mov_b32_e32 v50, v54
	v_mov_b32_e32 v51, v62
	v_mov_b32_e32 v62, v55
	v_mov_b32_e32 v54, v66
	v_mov_b32_e32 v55, v74
	v_mov_b32_e32 v74, v67
	v_mov_b32_e32 v66, v70
	v_mov_b32_e32 v67, v78
	v_mov_b32_e32 v78, v71
	v_mov_b32_e32 v70, v82
	v_mov_b32_e32 v71, v90
	v_pk_mul_f32 v[32:33], v[170:171], v[32:33] op_sel_hi:[0,1]
	v_pk_mul_f32 v[56:57], v[170:171], v[56:57] op_sel_hi:[0,1]
	v_pk_mul_f32 v[72:73], v[170:171], v[72:73] op_sel_hi:[0,1]
	v_pk_mul_f32 v[88:89], v[170:171], v[88:89] op_sel_hi:[0,1]
	v_pk_mul_f32 v[104:105], v[170:171], v[104:105] op_sel_hi:[0,1]
	v_pk_mul_f32 v[120:121], v[170:171], v[120:121] op_sel_hi:[0,1]
	v_pk_mul_f32 v[136:137], v[170:171], v[136:137] op_sel_hi:[0,1]
	v_pk_mul_f32 v[148:149], v[170:171], v[152:153] op_sel_hi:[0,1]
	v_mov_b32_e32 v90, v83
	v_mov_b32_e32 v82, v86
	v_mov_b32_e32 v83, v94
	v_mov_b32_e32 v94, v87
	v_mov_b32_e32 v86, v98
	v_mov_b32_e32 v87, v106
	v_mov_b32_e32 v106, v99
	v_mov_b32_e32 v98, v102
	v_mov_b32_e32 v99, v110
	v_mov_b32_e32 v110, v103
	v_mov_b32_e32 v102, v114
	v_mov_b32_e32 v103, v122
	v_mov_b32_e32 v122, v115
	v_mov_b32_e32 v114, v118
	v_mov_b32_e32 v115, v126
	v_mov_b32_e32 v126, v119
	v_mov_b32_e32 v118, v130
	v_mov_b32_e32 v119, v138
	v_mov_b32_e32 v138, v131
	v_mov_b32_e32 v130, v134
	v_mov_b32_e32 v131, v142
	v_mov_b32_e32 v142, v135
	v_mov_b32_e32 v134, v146
	v_mov_b32_e32 v135, v154
	v_pk_fma_f32 v[32:33], v[168:169], v[36:37], v[32:33] op_sel_hi:[0,1,1]
	v_pk_fma_f32 v[30:31], v[168:169], v[30:31], v[56:57] op_sel_hi:[0,1,1]
	v_pk_fma_f32 v[36:37], v[168:169], v[52:53], v[72:73] op_sel_hi:[0,1,1]
	v_pk_fma_f32 v[52:53], v[168:169], v[68:69], v[88:89] op_sel_hi:[0,1,1]
	v_pk_fma_f32 v[56:57], v[168:169], v[84:85], v[104:105] op_sel_hi:[0,1,1]
	v_pk_fma_f32 v[68:69], v[168:169], v[100:101], v[120:121] op_sel_hi:[0,1,1]
	v_pk_fma_f32 v[72:73], v[168:169], v[116:117], v[136:137] op_sel_hi:[0,1,1]
	v_pk_fma_f32 v[84:85], v[168:169], v[132:133], v[148:149] op_sel_hi:[0,1,1]
	v_mov_b32_e32 v169, v170
	v_mov_b32_e32 v154, v147
	v_pk_fma_f32 v[24:25], v[172:173], v[24:25], v[32:33] op_sel_hi:[0,1,1]
	v_pk_fma_f32 v[30:31], v[172:173], v[42:43], v[30:31] op_sel_hi:[0,1,1]
	v_pk_fma_f32 v[32:33], v[172:173], v[54:55], v[36:37] op_sel_hi:[0,1,1]
	v_pk_fma_f32 v[36:37], v[172:173], v[70:71], v[52:53] op_sel_hi:[0,1,1]
	v_pk_fma_f32 v[42:43], v[172:173], v[86:87], v[56:57] op_sel_hi:[0,1,1]
	v_pk_fma_f32 v[52:53], v[172:173], v[102:103], v[68:69] op_sel_hi:[0,1,1]
	v_pk_fma_f32 v[54:55], v[172:173], v[118:119], v[72:73] op_sel_hi:[0,1,1]
	v_pk_fma_f32 v[56:57], v[172:173], v[134:135], v[84:85] op_sel_hi:[0,1,1]
	s_waitcnt lgkmcnt(1)
	v_pk_mul_f32 v[68:69], v[168:169], v[160:161]
	v_mov_b32_e32 v173, v174
	v_pk_fma_f32 v[24:25], v[174:175], v[34:35], v[24:25] op_sel_hi:[0,1,1]
	v_pk_fma_f32 v[30:31], v[174:175], v[58:59], v[30:31] op_sel_hi:[0,1,1]
	v_pk_fma_f32 v[32:33], v[174:175], v[74:75], v[32:33] op_sel_hi:[0,1,1]
	v_pk_fma_f32 v[34:35], v[174:175], v[90:91], v[36:37] op_sel_hi:[0,1,1]
	v_pk_fma_f32 v[36:37], v[174:175], v[106:107], v[42:43] op_sel_hi:[0,1,1]
	v_pk_fma_f32 v[42:43], v[174:175], v[122:123], v[52:53] op_sel_hi:[0,1,1]
	v_pk_fma_f32 v[52:53], v[174:175], v[138:139], v[54:55] op_sel_hi:[0,1,1]
	v_pk_fma_f32 v[54:55], v[174:175], v[154:155], v[56:57] op_sel_hi:[0,1,1]
	v_pk_mul_f32 v[56:57], v[172:173], v[162:163]
	v_add_f32_e32 v58, v68, v69
	v_pk_fma_f32 v[24:25], v[176:177], v[26:27], v[24:25] op_sel_hi:[0,1,1]
	v_pk_fma_f32 v[26:27], v[176:177], v[48:49], v[30:31] op_sel_hi:[0,1,1]
	v_pk_fma_f32 v[30:31], v[176:177], v[64:65], v[32:33] op_sel_hi:[0,1,1]
	v_pk_fma_f32 v[32:33], v[176:177], v[80:81], v[34:35] op_sel_hi:[0,1,1]
	v_pk_fma_f32 v[34:35], v[176:177], v[96:97], v[36:37] op_sel_hi:[0,1,1]
	v_pk_fma_f32 v[36:37], v[176:177], v[112:113], v[42:43] op_sel_hi:[0,1,1]
	v_pk_fma_f32 v[42:43], v[176:177], v[128:129], v[52:53] op_sel_hi:[0,1,1]
	v_pk_fma_f32 v[48:49], v[176:177], v[144:145], v[54:55] op_sel_hi:[0,1,1]
	v_mov_b32_e32 v177, v178
	v_add_f32_e32 v52, v56, v58
	v_mov_b32_e32 v146, v150
	v_mov_b32_e32 v147, v158
	v_pk_fma_f32 v[24:25], v[178:179], v[44:45], v[24:25] op_sel_hi:[0,1,1]
	v_pk_fma_f32 v[26:27], v[178:179], v[60:61], v[26:27] op_sel_hi:[0,1,1]
	v_pk_fma_f32 v[30:31], v[178:179], v[76:77], v[30:31] op_sel_hi:[0,1,1]
	v_pk_fma_f32 v[32:33], v[178:179], v[92:93], v[32:33] op_sel_hi:[0,1,1]
	v_pk_fma_f32 v[34:35], v[178:179], v[108:109], v[34:35] op_sel_hi:[0,1,1]
	v_pk_fma_f32 v[36:37], v[178:179], v[124:125], v[36:37] op_sel_hi:[0,1,1]
	v_pk_fma_f32 v[42:43], v[178:179], v[140:141], v[42:43] op_sel_hi:[0,1,1]
	v_pk_fma_f32 v[44:45], v[178:179], v[156:157], v[48:49] op_sel_hi:[0,1,1]
	s_waitcnt lgkmcnt(0)
; #define LAS __attribute__((address_space(3)))
; __device__ __forceinline__ void p0_prologue(const Frame& F) {
;     ...
;             for (int k = 0; k < 128; k += 8) {
;                 float w[8];
; #pragma unroll
;                 for (int q = 0; q < 8; ++q) w[q] = wm[(size_t)(k + q) * 6144];
; #pragma unroll
;                 for (int r = 0; r < 17; ++r) { const f32x4 s0 = *(LAS const f32x4*)(S + r * 1024 + 128 * wave + k), s1 = *(LAS const f32x4*)(S + r * 1024 + 128 * wave + k + 4);
;                     acc[r] += s0[0] * w[0] + s0[1] * w[1] + s0[2] * w[2] + s0[3] * w[3] + s1[0] * w[4] + s1[1] * w[5] + s1[2] * w[6] + s1[3] * w[7]; }
	v_pk_mul_f32 v[48:49], v[176:177], v[164:165]
	v_add_f32_e32 v52, v57, v52
	v_mov_b32_e32 v158, v151
	v_pk_fma_f32 v[24:25], v[180:181], v[28:29], v[24:25] op_sel_hi:[0,1,1]
	v_pk_fma_f32 v[26:27], v[180:181], v[50:51], v[26:27] op_sel_hi:[0,1,1]
	v_pk_fma_f32 v[28:29], v[180:181], v[66:67], v[30:31] op_sel_hi:[0,1,1]
	v_pk_fma_f32 v[30:31], v[180:181], v[82:83], v[32:33] op_sel_hi:[0,1,1]
	v_pk_fma_f32 v[32:33], v[180:181], v[98:99], v[34:35] op_sel_hi:[0,1,1]
	v_pk_fma_f32 v[34:35], v[180:181], v[114:115], v[36:37] op_sel_hi:[0,1,1]
	v_pk_fma_f32 v[36:37], v[180:181], v[130:131], v[42:43] op_sel_hi:[0,1,1]
	v_pk_fma_f32 v[42:43], v[180:181], v[146:147], v[44:45] op_sel_hi:[0,1,1]
	v_mov_b32_e32 v181, v2
	v_add_f32_e32 v48, v48, v52
	v_pk_fma_f32 v[24:25], v[2:3], v[46:47], v[24:25] op_sel_hi:[0,1,1]
	v_pk_fma_f32 v[26:27], v[2:3], v[62:63], v[26:27] op_sel_hi:[0,1,1]
	v_pk_fma_f32 v[28:29], v[2:3], v[78:79], v[28:29] op_sel_hi:[0,1,1]
	v_pk_fma_f32 v[30:31], v[2:3], v[94:95], v[30:31] op_sel_hi:[0,1,1]
	v_pk_fma_f32 v[32:33], v[2:3], v[110:111], v[32:33] op_sel_hi:[0,1,1]
	v_pk_fma_f32 v[34:35], v[2:3], v[126:127], v[34:35] op_sel_hi:[0,1,1]
	v_pk_fma_f32 v[36:37], v[2:3], v[142:143], v[36:37] op_sel_hi:[0,1,1]
	v_pk_fma_f32 v[42:43], v[2:3], v[158:159], v[42:43] op_sel_hi:[0,1,1]
	v_pk_mul_f32 v[44:45], v[180:181], v[166:167]
	v_add_f32_e32 v2, v49, v48
	v_add_f32_e32 v2, v44, v2
	s_add_i32 s11, s11, 32
	v_add_f32_e32 v2, v45, v2
	v_pk_add_f32 v[8:9], v[8:9], v[24:25]
	v_pk_add_f32 v[10:11], v[10:11], v[26:27]
	v_pk_add_f32 v[12:13], v[12:13], v[28:29]
	v_pk_add_f32 v[14:15], v[14:15], v[30:31]
	v_pk_add_f32 v[16:17], v[16:17], v[32:33]
	v_pk_add_f32 v[18:19], v[18:19], v[34:35]
	v_pk_add_f32 v[20:21], v[20:21], v[36:37]
	v_pk_add_f32 v[22:23], v[22:23], v[42:43]
	v_add_f32_e32 v41, v41, v2
	s_waitcnt vmcnt(24)
	v_mov_b32_e32 v2, v206
	v_mov_b32_e32 v168, v207
	v_mov_b32_e32 v170, v208
	v_mov_b32_e32 v172, v209
	v_mov_b32_e32 v174, v210
	v_mov_b32_e32 v176, v211
	v_mov_b32_e32 v178, v212
	v_mov_b32_e32 v180, v213
	v_mov_b32_e32 v42, s11
	s_add_i32 s10, s10, 8
	v_add_co_u32_e64 v24, s[4:5], s19, v6
	global_load_dword v206, v[6:7], off
	s_nop 1
	v_addc_co_u32_e64 v25, s[4:5], -1, v7, s[4:5]
	v_add_co_u32_e64 v26, s[4:5], s20, v6
	s_nop 1
	v_addc_co_u32_e64 v27, s[4:5], -1, v7, s[4:5]
	v_add_co_u32_e64 v28, s[4:5], s21, v6
	s_nop 1
	v_addc_co_u32_e64 v29, s[4:5], -1, v7, s[4:5]
	v_add_co_u32_e64 v30, s[4:5], s22, v6
	s_nop 1
	v_addc_co_u32_e64 v31, s[4:5], -1, v7, s[4:5]
	v_add_co_u32_e64 v32, s[4:5], s23, v6
	s_nop 1
	v_addc_co_u32_e64 v33, s[4:5], -1, v7, s[4:5]
	v_add_co_u32_e64 v34, s[4:5], s27, v6
	s_nop 1
	v_addc_co_u32_e64 v35, s[4:5], -1, v7, s[4:5]
	v_add_co_u32_e64 v36, s[4:5], s28, v6
	s_nop 1
	v_addc_co_u32_e64 v37, s[4:5], -1, v7, s[4:5]
	global_load_dword v207, v[24:25], off
	global_load_dword v208, v[26:27], off
	global_load_dword v209, v[28:29], off
	global_load_dword v210, v[30:31], off
	global_load_dword v211, v[32:33], off
	global_load_dword v212, v[34:35], off
	global_load_dword v213, v[36:37], off
	v_lshl_add_u64 v[6:7], v[6:7], 0, s[6:7]
	ds_read_b128 v[24:27], v42
	ds_read_b128 v[28:31], v42 offset:16
	ds_read_b128 v[32:35], v42 offset:4096
	ds_read_b128 v[44:47], v42 offset:4112
	ds_read_b128 v[48:51], v42 offset:8192
	ds_read_b128 v[52:55], v42 offset:8208
	ds_read_b128 v[56:59], v42 offset:12288
	ds_read_b128 v[60:63], v42 offset:12304
	ds_read_b128 v[64:67], v42 offset:16384
	ds_read_b128 v[68:71], v42 offset:16400
	ds_read_b128 v[72:75], v42 offset:20480
	ds_read_b128 v[76:79], v42 offset:20496
	ds_read_b128 v[80:83], v42 offset:24576
	ds_read_b128 v[84:87], v42 offset:24592
	ds_read_b128 v[88:91], v42 offset:28672
	ds_read_b128 v[92:95], v42 offset:28688
	ds_read_b128 v[96:99], v42 offset:32768
	ds_read_b128 v[100:103], v42 offset:32784
	ds_read_b128 v[104:107], v42 offset:36864
	ds_read_b128 v[108:111], v42 offset:36880
	ds_read_b128 v[112:115], v42 offset:40960
	ds_read_b128 v[116:119], v42 offset:40976
	ds_read_b128 v[120:123], v42 offset:45056
	ds_read_b128 v[124:127], v42 offset:45072
	ds_read_b128 v[128:131], v42 offset:49152
	ds_read_b128 v[132:135], v42 offset:49168
	ds_read_b128 v[136:139], v42 offset:53248
	ds_read_b128 v[140:143], v42 offset:53264
	ds_read_b128 v[144:147], v42 offset:57344
	ds_read_b128 v[148:151], v42 offset:57360
	ds_read_b128 v[152:155], v42 offset:61440
	ds_read_b128 v[156:159], v42 offset:61456
	s_add_i32 s4, s11, 0x10000
	s_add_i32 s5, s11, 0x10010
	v_mov_b32_e32 v36, s4
	v_mov_b32_e32 v37, s5
	ds_read_b128 v[160:163], v36
	ds_read_b128 v[164:167], v37
	s_waitcnt lgkmcnt(14)
	v_mov_b32_e32 v37, v32
	v_mov_b32_e32 v32, v25
	v_mov_b32_e32 v25, v34
	v_mov_b32_e32 v34, v27
	v_mov_b32_e32 v27, v44
	v_mov_b32_e32 v44, v29
	v_mov_b32_e32 v29, v46
	v_mov_b32_e32 v46, v31
	v_mov_b32_e32 v31, v56
	v_mov_b32_e32 v56, v49
	v_mov_b32_e32 v49, v60
	v_mov_b32_e32 v60, v53
	v_mov_b32_e32 v53, v72
	v_mov_b32_e32 v72, v65
	v_mov_b32_e32 v65, v76
	v_mov_b32_e32 v76, v69
	v_mov_b32_e32 v69, v88
	v_mov_b32_e32 v88, v81
	v_mov_b32_e32 v81, v92
	v_mov_b32_e32 v92, v85
	v_mov_b32_e32 v85, v104
	v_mov_b32_e32 v104, v97
	v_mov_b32_e32 v97, v108
	v_mov_b32_e32 v108, v101
	s_waitcnt lgkmcnt(11)
	v_mov_b32_e32 v101, v120
	v_mov_b32_e32 v120, v113
	s_waitcnt lgkmcnt(10)
	v_mov_b32_e32 v113, v124
	v_mov_b32_e32 v124, v117
	s_waitcnt lgkmcnt(7)
	v_mov_b32_e32 v117, v136
	v_mov_b32_e32 v136, v129
	s_waitcnt lgkmcnt(6)
	v_mov_b32_e32 v129, v140
	v_mov_b32_e32 v140, v133
	s_waitcnt lgkmcnt(3)
; #define LAS __attribute__((address_space(3)))
; __device__ __forceinline__ void p0_prologue(const Frame& F) {
;     ...
;             for (int k = 0; k < 128; k += 8) {
;                 float w[8];
; #pragma unroll
;                 for (int q = 0; q < 8; ++q) w[q] = wm[(size_t)(k + q) * 6144];
; #pragma unroll
;                 for (int r = 0; r < 17; ++r) { const f32x4 s0 = *(LAS const f32x4*)(S + r * 1024 + 128 * wave + k), s1 = *(LAS const f32x4*)(S + r * 1024 + 128 * wave + k + 4);
;                     acc[r] += s0[0] * w[0] + s0[1] * w[1] + s0[2] * w[2] + s0[3] * w[3] + s1[0] * w[4] + s1[1] * w[5] + s1[2] * w[6] + s1[3] * w[7]; }
	v_mov_b32_e32 v133, v152
	v_mov_b32_e32 v152, v145
	v_mov_b32_e32 v36, v24
	v_mov_b32_e32 v24, v26
	v_mov_b32_e32 v26, v28
	v_mov_b32_e32 v28, v30
	v_mov_b32_e32 v30, v48
	v_mov_b32_e32 v48, v52
	v_mov_b32_e32 v52, v64
	v_mov_b32_e32 v64, v68
	v_mov_b32_e32 v68, v80
	v_mov_b32_e32 v80, v84
	v_mov_b32_e32 v84, v96
	v_mov_b32_e32 v96, v100
	v_mov_b32_e32 v100, v112
	v_mov_b32_e32 v112, v116
	v_mov_b32_e32 v116, v128
	v_mov_b32_e32 v128, v132
	v_mov_b32_e32 v132, v144
	v_mov_b32_e32 v144, v148
	s_waitcnt lgkmcnt(2)
	v_mov_b32_e32 v145, v156
	v_mov_b32_e32 v156, v149
	v_mov_b32_e32 v42, v50
	v_mov_b32_e32 v43, v58
	v_mov_b32_e32 v58, v51
	v_mov_b32_e32 v50, v54
	v_mov_b32_e32 v51, v62
	v_mov_b32_e32 v62, v55
	v_mov_b32_e32 v54, v66
	v_mov_b32_e32 v55, v74
	v_mov_b32_e32 v74, v67
	v_mov_b32_e32 v66, v70
	v_mov_b32_e32 v67, v78
	v_mov_b32_e32 v78, v71
	v_mov_b32_e32 v70, v82
	v_mov_b32_e32 v71, v90
	v_pk_mul_f32 v[32:33], v[170:171], v[32:33] op_sel_hi:[0,1]
	v_pk_mul_f32 v[56:57], v[170:171], v[56:57] op_sel_hi:[0,1]
	v_pk_mul_f32 v[72:73], v[170:171], v[72:73] op_sel_hi:[0,1]
	v_pk_mul_f32 v[88:89], v[170:171], v[88:89] op_sel_hi:[0,1]
	v_pk_mul_f32 v[104:105], v[170:171], v[104:105] op_sel_hi:[0,1]
	v_pk_mul_f32 v[120:121], v[170:171], v[120:121] op_sel_hi:[0,1]
	v_pk_mul_f32 v[136:137], v[170:171], v[136:137] op_sel_hi:[0,1]
	v_pk_mul_f32 v[148:149], v[170:171], v[152:153] op_sel_hi:[0,1]
	v_mov_b32_e32 v90, v83
	v_mov_b32_e32 v82, v86
	v_mov_b32_e32 v83, v94
	v_mov_b32_e32 v94, v87
	v_mov_b32_e32 v86, v98
	v_mov_b32_e32 v87, v106
	v_mov_b32_e32 v106, v99
	v_mov_b32_e32 v98, v102
	v_mov_b32_e32 v99, v110
	v_mov_b32_e32 v110, v103
	v_mov_b32_e32 v102, v114
	v_mov_b32_e32 v103, v122
	v_mov_b32_e32 v122, v115
	v_mov_b32_e32 v114, v118
	v_mov_b32_e32 v115, v126
	v_mov_b32_e32 v126, v119
	v_mov_b32_e32 v118, v130
	v_mov_b32_e32 v119, v138
	v_mov_b32_e32 v138, v131
	v_mov_b32_e32 v130, v134
	v_mov_b32_e32 v131, v142
	v_mov_b32_e32 v142, v135
	v_mov_b32_e32 v134, v146
	v_mov_b32_e32 v135, v154
	v_pk_fma_f32 v[32:33], v[168:169], v[36:37], v[32:33] op_sel_hi:[0,1,1]
	v_pk_fma_f32 v[30:31], v[168:169], v[30:31], v[56:57] op_sel_hi:[0,1,1]
	v_pk_fma_f32 v[36:37], v[168:169], v[52:53], v[72:73] op_sel_hi:[0,1,1]
	v_pk_fma_f32 v[52:53], v[168:169], v[68:69], v[88:89] op_sel_hi:[0,1,1]
	v_pk_fma_f32 v[56:57], v[168:169], v[84:85], v[104:105] op_sel_hi:[0,1,1]
	v_pk_fma_f32 v[68:69], v[168:169], v[100:101], v[120:121] op_sel_hi:[0,1,1]
	v_pk_fma_f32 v[72:73], v[168:169], v[116:117], v[136:137] op_sel_hi:[0,1,1]
	v_pk_fma_f32 v[84:85], v[168:169], v[132:133], v[148:149] op_sel_hi:[0,1,1]
	v_mov_b32_e32 v169, v170
	v_mov_b32_e32 v154, v147
	v_pk_fma_f32 v[24:25], v[172:173], v[24:25], v[32:33] op_sel_hi:[0,1,1]
	v_pk_fma_f32 v[30:31], v[172:173], v[42:43], v[30:31] op_sel_hi:[0,1,1]
	v_pk_fma_f32 v[32:33], v[172:173], v[54:55], v[36:37] op_sel_hi:[0,1,1]
	v_pk_fma_f32 v[36:37], v[172:173], v[70:71], v[52:53] op_sel_hi:[0,1,1]
	v_pk_fma_f32 v[42:43], v[172:173], v[86:87], v[56:57] op_sel_hi:[0,1,1]
	v_pk_fma_f32 v[52:53], v[172:173], v[102:103], v[68:69] op_sel_hi:[0,1,1]
	v_pk_fma_f32 v[54:55], v[172:173], v[118:119], v[72:73] op_sel_hi:[0,1,1]
	v_pk_fma_f32 v[56:57], v[172:173], v[134:135], v[84:85] op_sel_hi:[0,1,1]
	s_waitcnt lgkmcnt(1)
	v_pk_mul_f32 v[68:69], v[168:169], v[160:161]
	v_mov_b32_e32 v173, v174
	v_pk_fma_f32 v[24:25], v[174:175], v[34:35], v[24:25] op_sel_hi:[0,1,1]
	v_pk_fma_f32 v[30:31], v[174:175], v[58:59], v[30:31] op_sel_hi:[0,1,1]
	v_pk_fma_f32 v[32:33], v[174:175], v[74:75], v[32:33] op_sel_hi:[0,1,1]
	v_pk_fma_f32 v[34:35], v[174:175], v[90:91], v[36:37] op_sel_hi:[0,1,1]
	v_pk_fma_f32 v[36:37], v[174:175], v[106:107], v[42:43] op_sel_hi:[0,1,1]
	v_pk_fma_f32 v[42:43], v[174:175], v[122:123], v[52:53] op_sel_hi:[0,1,1]
	v_pk_fma_f32 v[52:53], v[174:175], v[138:139], v[54:55] op_sel_hi:[0,1,1]
	v_pk_fma_f32 v[54:55], v[174:175], v[154:155], v[56:57] op_sel_hi:[0,1,1]
	v_pk_mul_f32 v[56:57], v[172:173], v[162:163]
	v_add_f32_e32 v58, v68, v69
	v_pk_fma_f32 v[24:25], v[176:177], v[26:27], v[24:25] op_sel_hi:[0,1,1]
	v_pk_fma_f32 v[26:27], v[176:177], v[48:49], v[30:31] op_sel_hi:[0,1,1]
	v_pk_fma_f32 v[30:31], v[176:177], v[64:65], v[32:33] op_sel_hi:[0,1,1]
	v_pk_fma_f32 v[32:33], v[176:177], v[80:81], v[34:35] op_sel_hi:[0,1,1]
	v_pk_fma_f32 v[34:35], v[176:177], v[96:97], v[36:37] op_sel_hi:[0,1,1]
	v_pk_fma_f32 v[36:37], v[176:177], v[112:113], v[42:43] op_sel_hi:[0,1,1]
	v_pk_fma_f32 v[42:43], v[176:177], v[128:129], v[52:53] op_sel_hi:[0,1,1]
	v_pk_fma_f32 v[48:49], v[176:177], v[144:145], v[54:55] op_sel_hi:[0,1,1]
	v_mov_b32_e32 v177, v178
	v_add_f32_e32 v52, v56, v58
	v_mov_b32_e32 v146, v150
	v_mov_b32_e32 v147, v158
	v_pk_fma_f32 v[24:25], v[178:179], v[44:45], v[24:25] op_sel_hi:[0,1,1]
	v_pk_fma_f32 v[26:27], v[178:179], v[60:61], v[26:27] op_sel_hi:[0,1,1]
	v_pk_fma_f32 v[30:31], v[178:179], v[76:77], v[30:31] op_sel_hi:[0,1,1]
	v_pk_fma_f32 v[32:33], v[178:179], v[92:93], v[32:33] op_sel_hi:[0,1,1]
	v_pk_fma_f32 v[34:35], v[178:179], v[108:109], v[34:35] op_sel_hi:[0,1,1]
	v_pk_fma_f32 v[36:37], v[178:179], v[124:125], v[36:37] op_sel_hi:[0,1,1]
	v_pk_fma_f32 v[42:43], v[178:179], v[140:141], v[42:43] op_sel_hi:[0,1,1]
	v_pk_fma_f32 v[44:45], v[178:179], v[156:157], v[48:49] op_sel_hi:[0,1,1]
	s_waitcnt lgkmcnt(0)
; #define LAS __attribute__((address_space(3)))
; __device__ __forceinline__ void p0_prologue(const Frame& F) {
;     ...
;             for (int k = 0; k < 128; k += 8) {
;                 float w[8];
; #pragma unroll
;                 for (int q = 0; q < 8; ++q) w[q] = wm[(size_t)(k + q) * 6144];
; #pragma unroll
;                 for (int r = 0; r < 17; ++r) { const f32x4 s0 = *(LAS const f32x4*)(S + r * 1024 + 128 * wave + k), s1 = *(LAS const f32x4*)(S + r * 1024 + 128 * wave + k + 4);
;                     acc[r] += s0[0] * w[0] + s0[1] * w[1] + s0[2] * w[2] + s0[3] * w[3] + s1[0] * w[4] + s1[1] * w[5] + s1[2] * w[6] + s1[3] * w[7]; }
	v_pk_mul_f32 v[48:49], v[176:177], v[164:165]
	v_add_f32_e32 v52, v57, v52
	v_mov_b32_e32 v158, v151
	v_pk_fma_f32 v[24:25], v[180:181], v[28:29], v[24:25] op_sel_hi:[0,1,1]
	v_pk_fma_f32 v[26:27], v[180:181], v[50:51], v[26:27] op_sel_hi:[0,1,1]
	v_pk_fma_f32 v[28:29], v[180:181], v[66:67], v[30:31] op_sel_hi:[0,1,1]
	v_pk_fma_f32 v[30:31], v[180:181], v[82:83], v[32:33] op_sel_hi:[0,1,1]
	v_pk_fma_f32 v[32:33], v[180:181], v[98:99], v[34:35] op_sel_hi:[0,1,1]
	v_pk_fma_f32 v[34:35], v[180:181], v[114:115], v[36:37] op_sel_hi:[0,1,1]
	v_pk_fma_f32 v[36:37], v[180:181], v[130:131], v[42:43] op_sel_hi:[0,1,1]
	v_pk_fma_f32 v[42:43], v[180:181], v[146:147], v[44:45] op_sel_hi:[0,1,1]
	v_mov_b32_e32 v181, v2
	v_add_f32_e32 v48, v48, v52
	v_pk_fma_f32 v[24:25], v[2:3], v[46:47], v[24:25] op_sel_hi:[0,1,1]
	v_pk_fma_f32 v[26:27], v[2:3], v[62:63], v[26:27] op_sel_hi:[0,1,1]
	v_pk_fma_f32 v[28:29], v[2:3], v[78:79], v[28:29] op_sel_hi:[0,1,1]
	v_pk_fma_f32 v[30:31], v[2:3], v[94:95], v[30:31] op_sel_hi:[0,1,1]
	v_pk_fma_f32 v[32:33], v[2:3], v[110:111], v[32:33] op_sel_hi:[0,1,1]
	v_pk_fma_f32 v[34:35], v[2:3], v[126:127], v[34:35] op_sel_hi:[0,1,1]
	v_pk_fma_f32 v[36:37], v[2:3], v[142:143], v[36:37] op_sel_hi:[0,1,1]
	v_pk_fma_f32 v[42:43], v[2:3], v[158:159], v[42:43] op_sel_hi:[0,1,1]
	v_pk_mul_f32 v[44:45], v[180:181], v[166:167]
	v_add_f32_e32 v2, v49, v48
	v_add_f32_e32 v2, v44, v2
	s_add_i32 s11, s11, 32
	v_add_f32_e32 v2, v45, v2
	v_pk_add_f32 v[8:9], v[8:9], v[24:25]
	v_pk_add_f32 v[10:11], v[10:11], v[26:27]
	v_pk_add_f32 v[12:13], v[12:13], v[28:29]
	v_pk_add_f32 v[14:15], v[14:15], v[30:31]
	v_pk_add_f32 v[16:17], v[16:17], v[32:33]
	v_pk_add_f32 v[18:19], v[18:19], v[34:35]
	v_pk_add_f32 v[20:21], v[20:21], v[36:37]
	v_pk_add_f32 v[22:23], v[22:23], v[42:43]
	v_add_f32_e32 v41, v41, v2
	s_cmpk_gt_u32 s10, 0x57
	s_cbranch_scc0 .LBB0_13
	s_waitcnt vmcnt(24)
	v_mov_b32_e32 v2, v182
	v_mov_b32_e32 v168, v183
	v_mov_b32_e32 v170, v184
	v_mov_b32_e32 v172, v185
	v_mov_b32_e32 v174, v186
	v_mov_b32_e32 v176, v187
	v_mov_b32_e32 v178, v188
	v_mov_b32_e32 v180, v189
	v_mov_b32_e32 v42, s11
	s_add_i32 s10, s10, 8
	ds_read_b128 v[24:27], v42
	ds_read_b128 v[28:31], v42 offset:16
	ds_read_b128 v[32:35], v42 offset:4096
	ds_read_b128 v[44:47], v42 offset:4112
	ds_read_b128 v[48:51], v42 offset:8192
	ds_read_b128 v[52:55], v42 offset:8208
	ds_read_b128 v[56:59], v42 offset:12288
	ds_read_b128 v[60:63], v42 offset:12304
	ds_read_b128 v[64:67], v42 offset:16384
	ds_read_b128 v[68:71], v42 offset:16400
	ds_read_b128 v[72:75], v42 offset:20480
	ds_read_b128 v[76:79], v42 offset:20496
	ds_read_b128 v[80:83], v42 offset:24576
	ds_read_b128 v[84:87], v42 offset:24592
	ds_read_b128 v[88:91], v42 offset:28672
	ds_read_b128 v[92:95], v42 offset:28688
	ds_read_b128 v[96:99], v42 offset:32768
	ds_read_b128 v[100:103], v42 offset:32784
	ds_read_b128 v[104:107], v42 offset:36864
	ds_read_b128 v[108:111], v42 offset:36880
	ds_read_b128 v[112:115], v42 offset:40960
	ds_read_b128 v[116:119], v42 offset:40976
	ds_read_b128 v[120:123], v42 offset:45056
	ds_read_b128 v[124:127], v42 offset:45072
	ds_read_b128 v[128:131], v42 offset:49152
	ds_read_b128 v[132:135], v42 offset:49168
	ds_read_b128 v[136:139], v42 offset:53248
	ds_read_b128 v[140:143], v42 offset:53264
	ds_read_b128 v[144:147], v42 offset:57344
	ds_read_b128 v[148:151], v42 offset:57360
	ds_read_b128 v[152:155], v42 offset:61440
	ds_read_b128 v[156:159], v42 offset:61456
	s_add_i32 s4, s11, 0x10000
	s_add_i32 s5, s11, 0x10010
	v_mov_b32_e32 v36, s4
	v_mov_b32_e32 v37, s5
	ds_read_b128 v[160:163], v36
	ds_read_b128 v[164:167], v37
	s_waitcnt lgkmcnt(14)
	v_mov_b32_e32 v37, v32
	v_mov_b32_e32 v32, v25
	v_mov_b32_e32 v25, v34
	v_mov_b32_e32 v34, v27
	v_mov_b32_e32 v27, v44
	v_mov_b32_e32 v44, v29
	v_mov_b32_e32 v29, v46
	v_mov_b32_e32 v46, v31
	v_mov_b32_e32 v31, v56
	v_mov_b32_e32 v56, v49
	v_mov_b32_e32 v49, v60
	v_mov_b32_e32 v60, v53
	v_mov_b32_e32 v53, v72
	v_mov_b32_e32 v72, v65
	v_mov_b32_e32 v65, v76
	v_mov_b32_e32 v76, v69
	v_mov_b32_e32 v69, v88
	v_mov_b32_e32 v88, v81
	v_mov_b32_e32 v81, v92
	v_mov_b32_e32 v92, v85
	v_mov_b32_e32 v85, v104
	v_mov_b32_e32 v104, v97
	v_mov_b32_e32 v97, v108
	v_mov_b32_e32 v108, v101
	s_waitcnt lgkmcnt(11)
	v_mov_b32_e32 v101, v120
	v_mov_b32_e32 v120, v113
	s_waitcnt lgkmcnt(10)
	v_mov_b32_e32 v113, v124
	v_mov_b32_e32 v124, v117
	s_waitcnt lgkmcnt(7)
	v_mov_b32_e32 v117, v136
	v_mov_b32_e32 v136, v129
	s_waitcnt lgkmcnt(6)
	v_mov_b32_e32 v129, v140
	v_mov_b32_e32 v140, v133
	s_waitcnt lgkmcnt(3)
	v_mov_b32_e32 v133, v152
	v_mov_b32_e32 v152, v145
	v_mov_b32_e32 v36, v24
	v_mov_b32_e32 v24, v26
	v_mov_b32_e32 v26, v28
	v_mov_b32_e32 v28, v30
	v_mov_b32_e32 v30, v48
	v_mov_b32_e32 v48, v52
	v_mov_b32_e32 v52, v64
	v_mov_b32_e32 v64, v68
	v_mov_b32_e32 v68, v80
	v_mov_b32_e32 v80, v84
	v_mov_b32_e32 v84, v96
	v_mov_b32_e32 v96, v100
	v_mov_b32_e32 v100, v112
	v_mov_b32_e32 v112, v116
	v_mov_b32_e32 v116, v128
	v_mov_b32_e32 v128, v132
	v_mov_b32_e32 v132, v144
	v_mov_b32_e32 v144, v148
	s_waitcnt lgkmcnt(2)
; #define LAS __attribute__((address_space(3)))
; __device__ __forceinline__ void p0_prologue(const Frame& F) {
;     ...
;             for (int k = 0; k < 128; k += 8) {
;                 float w[8];
; #pragma unroll
;                 for (int q = 0; q < 8; ++q) w[q] = wm[(size_t)(k + q) * 6144];
; #pragma unroll
;                 for (int r = 0; r < 17; ++r) { const f32x4 s0 = *(LAS const f32x4*)(S + r * 1024 + 128 * wave + k), s1 = *(LAS const f32x4*)(S + r * 1024 + 128 * wave + k + 4);
;                     acc[r] += s0[0] * w[0] + s0[1] * w[1] + s0[2] * w[2] + s0[3] * w[3] + s1[0] * w[4] + s1[1] * w[5] + s1[2] * w[6] + s1[3] * w[7]; }
	v_mov_b32_e32 v145, v156
	v_mov_b32_e32 v156, v149
	v_mov_b32_e32 v42, v50
	v_mov_b32_e32 v43, v58
	v_mov_b32_e32 v58, v51
	v_mov_b32_e32 v50, v54
	v_mov_b32_e32 v51, v62
	v_mov_b32_e32 v62, v55
	v_mov_b32_e32 v54, v66
	v_mov_b32_e32 v55, v74
	v_mov_b32_e32 v74, v67
	v_mov_b32_e32 v66, v70
	v_mov_b32_e32 v67, v78
	v_mov_b32_e32 v78, v71
	v_mov_b32_e32 v70, v82
	v_mov_b32_e32 v71, v90
	v_pk_mul_f32 v[32:33], v[170:171], v[32:33] op_sel_hi:[0,1]
	v_pk_mul_f32 v[56:57], v[170:171], v[56:57] op_sel_hi:[0,1]
	v_pk_mul_f32 v[72:73], v[170:171], v[72:73] op_sel_hi:[0,1]
	v_pk_mul_f32 v[88:89], v[170:171], v[88:89] op_sel_hi:[0,1]
	v_pk_mul_f32 v[104:105], v[170:171], v[104:105] op_sel_hi:[0,1]
	v_pk_mul_f32 v[120:121], v[170:171], v[120:121] op_sel_hi:[0,1]
	v_pk_mul_f32 v[136:137], v[170:171], v[136:137] op_sel_hi:[0,1]
	v_pk_mul_f32 v[148:149], v[170:171], v[152:153] op_sel_hi:[0,1]
	v_mov_b32_e32 v90, v83
	v_mov_b32_e32 v82, v86
	v_mov_b32_e32 v83, v94
	v_mov_b32_e32 v94, v87
	v_mov_b32_e32 v86, v98
	v_mov_b32_e32 v87, v106
	v_mov_b32_e32 v106, v99
	v_mov_b32_e32 v98, v102
	v_mov_b32_e32 v99, v110
	v_mov_b32_e32 v110, v103
	v_mov_b32_e32 v102, v114
	v_mov_b32_e32 v103, v122
	v_mov_b32_e32 v122, v115
	v_mov_b32_e32 v114, v118
	v_mov_b32_e32 v115, v126
	v_mov_b32_e32 v126, v119
	v_mov_b32_e32 v118, v130
	v_mov_b32_e32 v119, v138
	v_mov_b32_e32 v138, v131
	v_mov_b32_e32 v130, v134
	v_mov_b32_e32 v131, v142
	v_mov_b32_e32 v142, v135
	v_mov_b32_e32 v134, v146
	v_mov_b32_e32 v135, v154
	v_pk_fma_f32 v[32:33], v[168:169], v[36:37], v[32:33] op_sel_hi:[0,1,1]
	v_pk_fma_f32 v[30:31], v[168:169], v[30:31], v[56:57] op_sel_hi:[0,1,1]
	v_pk_fma_f32 v[36:37], v[168:169], v[52:53], v[72:73] op_sel_hi:[0,1,1]
	v_pk_fma_f32 v[52:53], v[168:169], v[68:69], v[88:89] op_sel_hi:[0,1,1]
	v_pk_fma_f32 v[56:57], v[168:169], v[84:85], v[104:105] op_sel_hi:[0,1,1]
	v_pk_fma_f32 v[68:69], v[168:169], v[100:101], v[120:121] op_sel_hi:[0,1,1]
	v_pk_fma_f32 v[72:73], v[168:169], v[116:117], v[136:137] op_sel_hi:[0,1,1]
	v_pk_fma_f32 v[84:85], v[168:169], v[132:133], v[148:149] op_sel_hi:[0,1,1]
	v_mov_b32_e32 v169, v170
	v_mov_b32_e32 v154, v147
	v_pk_fma_f32 v[24:25], v[172:173], v[24:25], v[32:33] op_sel_hi:[0,1,1]
	v_pk_fma_f32 v[30:31], v[172:173], v[42:43], v[30:31] op_sel_hi:[0,1,1]
	v_pk_fma_f32 v[32:33], v[172:173], v[54:55], v[36:37] op_sel_hi:[0,1,1]
	v_pk_fma_f32 v[36:37], v[172:173], v[70:71], v[52:53] op_sel_hi:[0,1,1]
	v_pk_fma_f32 v[42:43], v[172:173], v[86:87], v[56:57] op_sel_hi:[0,1,1]
	v_pk_fma_f32 v[52:53], v[172:173], v[102:103], v[68:69] op_sel_hi:[0,1,1]
	v_pk_fma_f32 v[54:55], v[172:173], v[118:119], v[72:73] op_sel_hi:[0,1,1]
	v_pk_fma_f32 v[56:57], v[172:173], v[134:135], v[84:85] op_sel_hi:[0,1,1]
	s_waitcnt lgkmcnt(1)
	v_pk_mul_f32 v[68:69], v[168:169], v[160:161]
	v_mov_b32_e32 v173, v174
	v_pk_fma_f32 v[24:25], v[174:175], v[34:35], v[24:25] op_sel_hi:[0,1,1]
	v_pk_fma_f32 v[30:31], v[174:175], v[58:59], v[30:31] op_sel_hi:[0,1,1]
	v_pk_fma_f32 v[32:33], v[174:175], v[74:75], v[32:33] op_sel_hi:[0,1,1]
	v_pk_fma_f32 v[34:35], v[174:175], v[90:91], v[36:37] op_sel_hi:[0,1,1]
	v_pk_fma_f32 v[36:37], v[174:175], v[106:107], v[42:43] op_sel_hi:[0,1,1]
	v_pk_fma_f32 v[42:43], v[174:175], v[122:123], v[52:53] op_sel_hi:[0,1,1]
	v_pk_fma_f32 v[52:53], v[174:175], v[138:139], v[54:55] op_sel_hi:[0,1,1]
	v_pk_fma_f32 v[54:55], v[174:175], v[154:155], v[56:57] op_sel_hi:[0,1,1]
	v_pk_mul_f32 v[56:57], v[172:173], v[162:163]
	v_add_f32_e32 v58, v68, v69
	v_pk_fma_f32 v[24:25], v[176:177], v[26:27], v[24:25] op_sel_hi:[0,1,1]
	v_pk_fma_f32 v[26:27], v[176:177], v[48:49], v[30:31] op_sel_hi:[0,1,1]
	v_pk_fma_f32 v[30:31], v[176:177], v[64:65], v[32:33] op_sel_hi:[0,1,1]
	v_pk_fma_f32 v[32:33], v[176:177], v[80:81], v[34:35] op_sel_hi:[0,1,1]
	v_pk_fma_f32 v[34:35], v[176:177], v[96:97], v[36:37] op_sel_hi:[0,1,1]
	v_pk_fma_f32 v[36:37], v[176:177], v[112:113], v[42:43] op_sel_hi:[0,1,1]
	v_pk_fma_f32 v[42:43], v[176:177], v[128:129], v[52:53] op_sel_hi:[0,1,1]
	v_pk_fma_f32 v[48:49], v[176:177], v[144:145], v[54:55] op_sel_hi:[0,1,1]
	v_mov_b32_e32 v177, v178
	v_add_f32_e32 v52, v56, v58
	v_mov_b32_e32 v146, v150
	v_mov_b32_e32 v147, v158
	v_pk_fma_f32 v[24:25], v[178:179], v[44:45], v[24:25] op_sel_hi:[0,1,1]
	v_pk_fma_f32 v[26:27], v[178:179], v[60:61], v[26:27] op_sel_hi:[0,1,1]
	v_pk_fma_f32 v[30:31], v[178:179], v[76:77], v[30:31] op_sel_hi:[0,1,1]
	v_pk_fma_f32 v[32:33], v[178:179], v[92:93], v[32:33] op_sel_hi:[0,1,1]
	v_pk_fma_f32 v[34:35], v[178:179], v[108:109], v[34:35] op_sel_hi:[0,1,1]
	v_pk_fma_f32 v[36:37], v[178:179], v[124:125], v[36:37] op_sel_hi:[0,1,1]
	v_pk_fma_f32 v[42:43], v[178:179], v[140:141], v[42:43] op_sel_hi:[0,1,1]
	v_pk_fma_f32 v[44:45], v[178:179], v[156:157], v[48:49] op_sel_hi:[0,1,1]
	s_waitcnt lgkmcnt(0)
; #define LAS __attribute__((address_space(3)))
; __device__ __forceinline__ void p0_prologue(const Frame& F) {
;     ...
;             for (int k = 0; k < 128; k += 8) {
;                 float w[8];
; #pragma unroll
;                 for (int q = 0; q < 8; ++q) w[q] = wm[(size_t)(k + q) * 6144];
; #pragma unroll
;                 for (int r = 0; r < 17; ++r) { const f32x4 s0 = *(LAS const f32x4*)(S + r * 1024 + 128 * wave + k), s1 = *(LAS const f32x4*)(S + r * 1024 + 128 * wave + k + 4);
;                     acc[r] += s0[0] * w[0] + s0[1] * w[1] + s0[2] * w[2] + s0[3] * w[3] + s1[0] * w[4] + s1[1] * w[5] + s1[2] * w[6] + s1[3] * w[7]; }
	v_pk_mul_f32 v[48:49], v[176:177], v[164:165]
	v_add_f32_e32 v52, v57, v52
	v_mov_b32_e32 v158, v151
	v_pk_fma_f32 v[24:25], v[180:181], v[28:29], v[24:25] op_sel_hi:[0,1,1]
	v_pk_fma_f32 v[26:27], v[180:181], v[50:51], v[26:27] op_sel_hi:[0,1,1]
	v_pk_fma_f32 v[28:29], v[180:181], v[66:67], v[30:31] op_sel_hi:[0,1,1]
	v_pk_fma_f32 v[30:31], v[180:181], v[82:83], v[32:33] op_sel_hi:[0,1,1]
	v_pk_fma_f32 v[32:33], v[180:181], v[98:99], v[34:35] op_sel_hi:[0,1,1]
	v_pk_fma_f32 v[34:35], v[180:181], v[114:115], v[36:37] op_sel_hi:[0,1,1]
	v_pk_fma_f32 v[36:37], v[180:181], v[130:131], v[42:43] op_sel_hi:[0,1,1]
	v_pk_fma_f32 v[42:43], v[180:181], v[146:147], v[44:45] op_sel_hi:[0,1,1]
	v_mov_b32_e32 v181, v2
	v_add_f32_e32 v48, v48, v52
	v_pk_fma_f32 v[24:25], v[2:3], v[46:47], v[24:25] op_sel_hi:[0,1,1]
	v_pk_fma_f32 v[26:27], v[2:3], v[62:63], v[26:27] op_sel_hi:[0,1,1]
	v_pk_fma_f32 v[28:29], v[2:3], v[78:79], v[28:29] op_sel_hi:[0,1,1]
	v_pk_fma_f32 v[30:31], v[2:3], v[94:95], v[30:31] op_sel_hi:[0,1,1]
	v_pk_fma_f32 v[32:33], v[2:3], v[110:111], v[32:33] op_sel_hi:[0,1,1]
	v_pk_fma_f32 v[34:35], v[2:3], v[126:127], v[34:35] op_sel_hi:[0,1,1]
	v_pk_fma_f32 v[36:37], v[2:3], v[142:143], v[36:37] op_sel_hi:[0,1,1]
	v_pk_fma_f32 v[42:43], v[2:3], v[158:159], v[42:43] op_sel_hi:[0,1,1]
	v_pk_mul_f32 v[44:45], v[180:181], v[166:167]
	v_add_f32_e32 v2, v49, v48
	v_add_f32_e32 v2, v44, v2
	s_add_i32 s11, s11, 32
	v_add_f32_e32 v2, v45, v2
	v_pk_add_f32 v[8:9], v[8:9], v[24:25]
	v_pk_add_f32 v[10:11], v[10:11], v[26:27]
	v_pk_add_f32 v[12:13], v[12:13], v[28:29]
	v_pk_add_f32 v[14:15], v[14:15], v[30:31]
	v_pk_add_f32 v[16:17], v[16:17], v[32:33]
	v_pk_add_f32 v[18:19], v[18:19], v[34:35]
	v_pk_add_f32 v[20:21], v[20:21], v[36:37]
	v_pk_add_f32 v[22:23], v[22:23], v[42:43]
	v_add_f32_e32 v41, v41, v2
	s_waitcnt vmcnt(16)
	v_mov_b32_e32 v2, v190
	v_mov_b32_e32 v168, v191
	v_mov_b32_e32 v170, v192
	v_mov_b32_e32 v172, v193
	v_mov_b32_e32 v174, v194
	v_mov_b32_e32 v176, v195
	v_mov_b32_e32 v178, v196
	v_mov_b32_e32 v180, v197
	v_mov_b32_e32 v42, s11
	s_add_i32 s10, s10, 8
	ds_read_b128 v[24:27], v42
	ds_read_b128 v[28:31], v42 offset:16
	ds_read_b128 v[32:35], v42 offset:4096
	ds_read_b128 v[44:47], v42 offset:4112
	ds_read_b128 v[48:51], v42 offset:8192
	ds_read_b128 v[52:55], v42 offset:8208
	ds_read_b128 v[56:59], v42 offset:12288
	ds_read_b128 v[60:63], v42 offset:12304
	ds_read_b128 v[64:67], v42 offset:16384
	ds_read_b128 v[68:71], v42 offset:16400
	ds_read_b128 v[72:75], v42 offset:20480
	ds_read_b128 v[76:79], v42 offset:20496
	ds_read_b128 v[80:83], v42 offset:24576
	ds_read_b128 v[84:87], v42 offset:24592
	ds_read_b128 v[88:91], v42 offset:28672
	ds_read_b128 v[92:95], v42 offset:28688
	ds_read_b128 v[96:99], v42 offset:32768
	ds_read_b128 v[100:103], v42 offset:32784
	ds_read_b128 v[104:107], v42 offset:36864
	ds_read_b128 v[108:111], v42 offset:36880
	ds_read_b128 v[112:115], v42 offset:40960
	ds_read_b128 v[116:119], v42 offset:40976
	ds_read_b128 v[120:123], v42 offset:45056
	ds_read_b128 v[124:127], v42 offset:45072
	ds_read_b128 v[128:131], v42 offset:49152
	ds_read_b128 v[132:135], v42 offset:49168
	ds_read_b128 v[136:139], v42 offset:53248
	ds_read_b128 v[140:143], v42 offset:53264
	ds_read_b128 v[144:147], v42 offset:57344
	ds_read_b128 v[148:151], v42 offset:57360
	ds_read_b128 v[152:155], v42 offset:61440
	ds_read_b128 v[156:159], v42 offset:61456
	s_add_i32 s4, s11, 0x10000
	s_add_i32 s5, s11, 0x10010
	v_mov_b32_e32 v36, s4
	v_mov_b32_e32 v37, s5
	ds_read_b128 v[160:163], v36
	ds_read_b128 v[164:167], v37
	s_waitcnt lgkmcnt(14)
	v_mov_b32_e32 v37, v32
	v_mov_b32_e32 v32, v25
	v_mov_b32_e32 v25, v34
	v_mov_b32_e32 v34, v27
	v_mov_b32_e32 v27, v44
	v_mov_b32_e32 v44, v29
	v_mov_b32_e32 v29, v46
	v_mov_b32_e32 v46, v31
	v_mov_b32_e32 v31, v56
	v_mov_b32_e32 v56, v49
	v_mov_b32_e32 v49, v60
	v_mov_b32_e32 v60, v53
	v_mov_b32_e32 v53, v72
	v_mov_b32_e32 v72, v65
	v_mov_b32_e32 v65, v76
	v_mov_b32_e32 v76, v69
	v_mov_b32_e32 v69, v88
	v_mov_b32_e32 v88, v81
	v_mov_b32_e32 v81, v92
	v_mov_b32_e32 v92, v85
	v_mov_b32_e32 v85, v104
	v_mov_b32_e32 v104, v97
	v_mov_b32_e32 v97, v108
	v_mov_b32_e32 v108, v101
	s_waitcnt lgkmcnt(11)
	v_mov_b32_e32 v101, v120
	v_mov_b32_e32 v120, v113
	s_waitcnt lgkmcnt(10)
	v_mov_b32_e32 v113, v124
	v_mov_b32_e32 v124, v117
	s_waitcnt lgkmcnt(7)
	v_mov_b32_e32 v117, v136
	v_mov_b32_e32 v136, v129
	s_waitcnt lgkmcnt(6)
	v_mov_b32_e32 v129, v140
	v_mov_b32_e32 v140, v133
	s_waitcnt lgkmcnt(3)
	v_mov_b32_e32 v133, v152
	v_mov_b32_e32 v152, v145
	v_mov_b32_e32 v36, v24
	v_mov_b32_e32 v24, v26
	v_mov_b32_e32 v26, v28
	v_mov_b32_e32 v28, v30
	v_mov_b32_e32 v30, v48
	v_mov_b32_e32 v48, v52
	v_mov_b32_e32 v52, v64
	v_mov_b32_e32 v64, v68
	v_mov_b32_e32 v68, v80
	v_mov_b32_e32 v80, v84
	v_mov_b32_e32 v84, v96
	v_mov_b32_e32 v96, v100
	v_mov_b32_e32 v100, v112
	v_mov_b32_e32 v112, v116
	v_mov_b32_e32 v116, v128
	v_mov_b32_e32 v128, v132
	v_mov_b32_e32 v132, v144
	v_mov_b32_e32 v144, v148
	s_waitcnt lgkmcnt(2)
; #define LAS __attribute__((address_space(3)))
; __device__ __forceinline__ void p0_prologue(const Frame& F) {
;     ...
;             for (int k = 0; k < 128; k += 8) {
;                 float w[8];
; #pragma unroll
;                 for (int q = 0; q < 8; ++q) w[q] = wm[(size_t)(k + q) * 6144];
; #pragma unroll
;                 for (int r = 0; r < 17; ++r) { const f32x4 s0 = *(LAS const f32x4*)(S + r * 1024 + 128 * wave + k), s1 = *(LAS const f32x4*)(S + r * 1024 + 128 * wave + k + 4);
;                     acc[r] += s0[0] * w[0] + s0[1] * w[1] + s0[2] * w[2] + s0[3] * w[3] + s1[0] * w[4] + s1[1] * w[5] + s1[2] * w[6] + s1[3] * w[7]; }
	v_mov_b32_e32 v145, v156
	v_mov_b32_e32 v156, v149
	v_mov_b32_e32 v42, v50
	v_mov_b32_e32 v43, v58
	v_mov_b32_e32 v58, v51
	v_mov_b32_e32 v50, v54
	v_mov_b32_e32 v51, v62
	v_mov_b32_e32 v62, v55
	v_mov_b32_e32 v54, v66
	v_mov_b32_e32 v55, v74
	v_mov_b32_e32 v74, v67
	v_mov_b32_e32 v66, v70
	v_mov_b32_e32 v67, v78
	v_mov_b32_e32 v78, v71
	v_mov_b32_e32 v70, v82
	v_mov_b32_e32 v71, v90
	v_pk_mul_f32 v[32:33], v[170:171], v[32:33] op_sel_hi:[0,1]
	v_pk_mul_f32 v[56:57], v[170:171], v[56:57] op_sel_hi:[0,1]
	v_pk_mul_f32 v[72:73], v[170:171], v[72:73] op_sel_hi:[0,1]
	v_pk_mul_f32 v[88:89], v[170:171], v[88:89] op_sel_hi:[0,1]
	v_pk_mul_f32 v[104:105], v[170:171], v[104:105] op_sel_hi:[0,1]
	v_pk_mul_f32 v[120:121], v[170:171], v[120:121] op_sel_hi:[0,1]
	v_pk_mul_f32 v[136:137], v[170:171], v[136:137] op_sel_hi:[0,1]
	v_pk_mul_f32 v[148:149], v[170:171], v[152:153] op_sel_hi:[0,1]
	v_mov_b32_e32 v90, v83
	v_mov_b32_e32 v82, v86
	v_mov_b32_e32 v83, v94
	v_mov_b32_e32 v94, v87
	v_mov_b32_e32 v86, v98
	v_mov_b32_e32 v87, v106
	v_mov_b32_e32 v106, v99
	v_mov_b32_e32 v98, v102
	v_mov_b32_e32 v99, v110
	v_mov_b32_e32 v110, v103
	v_mov_b32_e32 v102, v114
	v_mov_b32_e32 v103, v122
	v_mov_b32_e32 v122, v115
	v_mov_b32_e32 v114, v118
	v_mov_b32_e32 v115, v126
	v_mov_b32_e32 v126, v119
	v_mov_b32_e32 v118, v130
	v_mov_b32_e32 v119, v138
	v_mov_b32_e32 v138, v131
	v_mov_b32_e32 v130, v134
	v_mov_b32_e32 v131, v142
	v_mov_b32_e32 v142, v135
	v_mov_b32_e32 v134, v146
	v_mov_b32_e32 v135, v154
	v_pk_fma_f32 v[32:33], v[168:169], v[36:37], v[32:33] op_sel_hi:[0,1,1]
	v_pk_fma_f32 v[30:31], v[168:169], v[30:31], v[56:57] op_sel_hi:[0,1,1]
	v_pk_fma_f32 v[36:37], v[168:169], v[52:53], v[72:73] op_sel_hi:[0,1,1]
	v_pk_fma_f32 v[52:53], v[168:169], v[68:69], v[88:89] op_sel_hi:[0,1,1]
	v_pk_fma_f32 v[56:57], v[168:169], v[84:85], v[104:105] op_sel_hi:[0,1,1]
	v_pk_fma_f32 v[68:69], v[168:169], v[100:101], v[120:121] op_sel_hi:[0,1,1]
	v_pk_fma_f32 v[72:73], v[168:169], v[116:117], v[136:137] op_sel_hi:[0,1,1]
	v_pk_fma_f32 v[84:85], v[168:169], v[132:133], v[148:149] op_sel_hi:[0,1,1]
	v_mov_b32_e32 v169, v170
	v_mov_b32_e32 v154, v147
	v_pk_fma_f32 v[24:25], v[172:173], v[24:25], v[32:33] op_sel_hi:[0,1,1]
	v_pk_fma_f32 v[30:31], v[172:173], v[42:43], v[30:31] op_sel_hi:[0,1,1]
	v_pk_fma_f32 v[32:33], v[172:173], v[54:55], v[36:37] op_sel_hi:[0,1,1]
	v_pk_fma_f32 v[36:37], v[172:173], v[70:71], v[52:53] op_sel_hi:[0,1,1]
	v_pk_fma_f32 v[42:43], v[172:173], v[86:87], v[56:57] op_sel_hi:[0,1,1]
	v_pk_fma_f32 v[52:53], v[172:173], v[102:103], v[68:69] op_sel_hi:[0,1,1]
	v_pk_fma_f32 v[54:55], v[172:173], v[118:119], v[72:73] op_sel_hi:[0,1,1]
	v_pk_fma_f32 v[56:57], v[172:173], v[134:135], v[84:85] op_sel_hi:[0,1,1]
	s_waitcnt lgkmcnt(1)
	v_pk_mul_f32 v[68:69], v[168:169], v[160:161]
	v_mov_b32_e32 v173, v174
	v_pk_fma_f32 v[24:25], v[174:175], v[34:35], v[24:25] op_sel_hi:[0,1,1]
	v_pk_fma_f32 v[30:31], v[174:175], v[58:59], v[30:31] op_sel_hi:[0,1,1]
	v_pk_fma_f32 v[32:33], v[174:175], v[74:75], v[32:33] op_sel_hi:[0,1,1]
	v_pk_fma_f32 v[34:35], v[174:175], v[90:91], v[36:37] op_sel_hi:[0,1,1]
	v_pk_fma_f32 v[36:37], v[174:175], v[106:107], v[42:43] op_sel_hi:[0,1,1]
	v_pk_fma_f32 v[42:43], v[174:175], v[122:123], v[52:53] op_sel_hi:[0,1,1]
	v_pk_fma_f32 v[52:53], v[174:175], v[138:139], v[54:55] op_sel_hi:[0,1,1]
	v_pk_fma_f32 v[54:55], v[174:175], v[154:155], v[56:57] op_sel_hi:[0,1,1]
	v_pk_mul_f32 v[56:57], v[172:173], v[162:163]
	v_add_f32_e32 v58, v68, v69
	v_pk_fma_f32 v[24:25], v[176:177], v[26:27], v[24:25] op_sel_hi:[0,1,1]
	v_pk_fma_f32 v[26:27], v[176:177], v[48:49], v[30:31] op_sel_hi:[0,1,1]
	v_pk_fma_f32 v[30:31], v[176:177], v[64:65], v[32:33] op_sel_hi:[0,1,1]
	v_pk_fma_f32 v[32:33], v[176:177], v[80:81], v[34:35] op_sel_hi:[0,1,1]
	v_pk_fma_f32 v[34:35], v[176:177], v[96:97], v[36:37] op_sel_hi:[0,1,1]
	v_pk_fma_f32 v[36:37], v[176:177], v[112:113], v[42:43] op_sel_hi:[0,1,1]
	v_pk_fma_f32 v[42:43], v[176:177], v[128:129], v[52:53] op_sel_hi:[0,1,1]
	v_pk_fma_f32 v[48:49], v[176:177], v[144:145], v[54:55] op_sel_hi:[0,1,1]
	v_mov_b32_e32 v177, v178
	v_add_f32_e32 v52, v56, v58
	v_mov_b32_e32 v146, v150
	v_mov_b32_e32 v147, v158
	v_pk_fma_f32 v[24:25], v[178:179], v[44:45], v[24:25] op_sel_hi:[0,1,1]
	v_pk_fma_f32 v[26:27], v[178:179], v[60:61], v[26:27] op_sel_hi:[0,1,1]
	v_pk_fma_f32 v[30:31], v[178:179], v[76:77], v[30:31] op_sel_hi:[0,1,1]
	v_pk_fma_f32 v[32:33], v[178:179], v[92:93], v[32:33] op_sel_hi:[0,1,1]
	v_pk_fma_f32 v[34:35], v[178:179], v[108:109], v[34:35] op_sel_hi:[0,1,1]
	v_pk_fma_f32 v[36:37], v[178:179], v[124:125], v[36:37] op_sel_hi:[0,1,1]
	v_pk_fma_f32 v[42:43], v[178:179], v[140:141], v[42:43] op_sel_hi:[0,1,1]
	v_pk_fma_f32 v[44:45], v[178:179], v[156:157], v[48:49] op_sel_hi:[0,1,1]
	s_waitcnt lgkmcnt(0)
; #define LAS __attribute__((address_space(3)))
; __device__ __forceinline__ void p0_prologue(const Frame& F) {
;     ...
;             for (int k = 0; k < 128; k += 8) {
;                 float w[8];
; #pragma unroll
;                 for (int q = 0; q < 8; ++q) w[q] = wm[(size_t)(k + q) * 6144];
; #pragma unroll
;                 for (int r = 0; r < 17; ++r) { const f32x4 s0 = *(LAS const f32x4*)(S + r * 1024 + 128 * wave + k), s1 = *(LAS const f32x4*)(S + r * 1024 + 128 * wave + k + 4);
;                     acc[r] += s0[0] * w[0] + s0[1] * w[1] + s0[2] * w[2] + s0[3] * w[3] + s1[0] * w[4] + s1[1] * w[5] + s1[2] * w[6] + s1[3] * w[7]; }
	v_pk_mul_f32 v[48:49], v[176:177], v[164:165]
	v_add_f32_e32 v52, v57, v52
	v_mov_b32_e32 v158, v151
	v_pk_fma_f32 v[24:25], v[180:181], v[28:29], v[24:25] op_sel_hi:[0,1,1]
	v_pk_fma_f32 v[26:27], v[180:181], v[50:51], v[26:27] op_sel_hi:[0,1,1]
	v_pk_fma_f32 v[28:29], v[180:181], v[66:67], v[30:31] op_sel_hi:[0,1,1]
	v_pk_fma_f32 v[30:31], v[180:181], v[82:83], v[32:33] op_sel_hi:[0,1,1]
	v_pk_fma_f32 v[32:33], v[180:181], v[98:99], v[34:35] op_sel_hi:[0,1,1]
	v_pk_fma_f32 v[34:35], v[180:181], v[114:115], v[36:37] op_sel_hi:[0,1,1]
	v_pk_fma_f32 v[36:37], v[180:181], v[130:131], v[42:43] op_sel_hi:[0,1,1]
	v_pk_fma_f32 v[42:43], v[180:181], v[146:147], v[44:45] op_sel_hi:[0,1,1]
	v_mov_b32_e32 v181, v2
	v_add_f32_e32 v48, v48, v52
	v_pk_fma_f32 v[24:25], v[2:3], v[46:47], v[24:25] op_sel_hi:[0,1,1]
	v_pk_fma_f32 v[26:27], v[2:3], v[62:63], v[26:27] op_sel_hi:[0,1,1]
	v_pk_fma_f32 v[28:29], v[2:3], v[78:79], v[28:29] op_sel_hi:[0,1,1]
	v_pk_fma_f32 v[30:31], v[2:3], v[94:95], v[30:31] op_sel_hi:[0,1,1]
	v_pk_fma_f32 v[32:33], v[2:3], v[110:111], v[32:33] op_sel_hi:[0,1,1]
	v_pk_fma_f32 v[34:35], v[2:3], v[126:127], v[34:35] op_sel_hi:[0,1,1]
	v_pk_fma_f32 v[36:37], v[2:3], v[142:143], v[36:37] op_sel_hi:[0,1,1]
	v_pk_fma_f32 v[42:43], v[2:3], v[158:159], v[42:43] op_sel_hi:[0,1,1]
	v_pk_mul_f32 v[44:45], v[180:181], v[166:167]
	v_add_f32_e32 v2, v49, v48
	v_add_f32_e32 v2, v44, v2
	s_add_i32 s11, s11, 32
	v_add_f32_e32 v2, v45, v2
	v_pk_add_f32 v[8:9], v[8:9], v[24:25]
	v_pk_add_f32 v[10:11], v[10:11], v[26:27]
	v_pk_add_f32 v[12:13], v[12:13], v[28:29]
	v_pk_add_f32 v[14:15], v[14:15], v[30:31]
	v_pk_add_f32 v[16:17], v[16:17], v[32:33]
	v_pk_add_f32 v[18:19], v[18:19], v[34:35]
	v_pk_add_f32 v[20:21], v[20:21], v[36:37]
	v_pk_add_f32 v[22:23], v[22:23], v[42:43]
	v_add_f32_e32 v41, v41, v2
	s_waitcnt vmcnt(8)
	v_mov_b32_e32 v2, v198
	v_mov_b32_e32 v168, v199
	v_mov_b32_e32 v170, v200
	v_mov_b32_e32 v172, v201
	v_mov_b32_e32 v174, v202
	v_mov_b32_e32 v176, v203
	v_mov_b32_e32 v178, v204
	v_mov_b32_e32 v180, v205
	v_mov_b32_e32 v42, s11
	s_add_i32 s10, s10, 8
	ds_read_b128 v[24:27], v42
	ds_read_b128 v[28:31], v42 offset:16
	ds_read_b128 v[32:35], v42 offset:4096
	ds_read_b128 v[44:47], v42 offset:4112
	ds_read_b128 v[48:51], v42 offset:8192
	ds_read_b128 v[52:55], v42 offset:8208
	ds_read_b128 v[56:59], v42 offset:12288
	ds_read_b128 v[60:63], v42 offset:12304
	ds_read_b128 v[64:67], v42 offset:16384
	ds_read_b128 v[68:71], v42 offset:16400
	ds_read_b128 v[72:75], v42 offset:20480
	ds_read_b128 v[76:79], v42 offset:20496
	ds_read_b128 v[80:83], v42 offset:24576
	ds_read_b128 v[84:87], v42 offset:24592
	ds_read_b128 v[88:91], v42 offset:28672
	ds_read_b128 v[92:95], v42 offset:28688
	ds_read_b128 v[96:99], v42 offset:32768
	ds_read_b128 v[100:103], v42 offset:32784
	ds_read_b128 v[104:107], v42 offset:36864
	ds_read_b128 v[108:111], v42 offset:36880
	ds_read_b128 v[112:115], v42 offset:40960
	ds_read_b128 v[116:119], v42 offset:40976
	ds_read_b128 v[120:123], v42 offset:45056
	ds_read_b128 v[124:127], v42 offset:45072
	ds_read_b128 v[128:131], v42 offset:49152
	ds_read_b128 v[132:135], v42 offset:49168
	ds_read_b128 v[136:139], v42 offset:53248
	ds_read_b128 v[140:143], v42 offset:53264
	ds_read_b128 v[144:147], v42 offset:57344
	ds_read_b128 v[148:151], v42 offset:57360
	ds_read_b128 v[152:155], v42 offset:61440
	ds_read_b128 v[156:159], v42 offset:61456
	s_add_i32 s4, s11, 0x10000
	s_add_i32 s5, s11, 0x10010
	v_mov_b32_e32 v36, s4
	v_mov_b32_e32 v37, s5
	ds_read_b128 v[160:163], v36
	ds_read_b128 v[164:167], v37
	s_waitcnt lgkmcnt(14)
	v_mov_b32_e32 v37, v32
	v_mov_b32_e32 v32, v25
	v_mov_b32_e32 v25, v34
	v_mov_b32_e32 v34, v27
	v_mov_b32_e32 v27, v44
	v_mov_b32_e32 v44, v29
	v_mov_b32_e32 v29, v46
	v_mov_b32_e32 v46, v31
	v_mov_b32_e32 v31, v56
	v_mov_b32_e32 v56, v49
	v_mov_b32_e32 v49, v60
	v_mov_b32_e32 v60, v53
	v_mov_b32_e32 v53, v72
	v_mov_b32_e32 v72, v65
	v_mov_b32_e32 v65, v76
	v_mov_b32_e32 v76, v69
	v_mov_b32_e32 v69, v88
	v_mov_b32_e32 v88, v81
	v_mov_b32_e32 v81, v92
	v_mov_b32_e32 v92, v85
	v_mov_b32_e32 v85, v104
	v_mov_b32_e32 v104, v97
	v_mov_b32_e32 v97, v108
	v_mov_b32_e32 v108, v101
	s_waitcnt lgkmcnt(11)
	v_mov_b32_e32 v101, v120
	v_mov_b32_e32 v120, v113
	s_waitcnt lgkmcnt(10)
	v_mov_b32_e32 v113, v124
	v_mov_b32_e32 v124, v117
	s_waitcnt lgkmcnt(7)
	v_mov_b32_e32 v117, v136
	v_mov_b32_e32 v136, v129
	s_waitcnt lgkmcnt(6)
	v_mov_b32_e32 v129, v140
	v_mov_b32_e32 v140, v133
	s_waitcnt lgkmcnt(3)
	v_mov_b32_e32 v133, v152
	v_mov_b32_e32 v152, v145
	v_mov_b32_e32 v36, v24
	v_mov_b32_e32 v24, v26
	v_mov_b32_e32 v26, v28
	v_mov_b32_e32 v28, v30
	v_mov_b32_e32 v30, v48
	v_mov_b32_e32 v48, v52
	v_mov_b32_e32 v52, v64
	v_mov_b32_e32 v64, v68
	v_mov_b32_e32 v68, v80
	v_mov_b32_e32 v80, v84
	v_mov_b32_e32 v84, v96
	v_mov_b32_e32 v96, v100
	v_mov_b32_e32 v100, v112
	v_mov_b32_e32 v112, v116
	v_mov_b32_e32 v116, v128
	v_mov_b32_e32 v128, v132
	v_mov_b32_e32 v132, v144
	v_mov_b32_e32 v144, v148
	s_waitcnt lgkmcnt(2)
; #define LAS __attribute__((address_space(3)))
; __device__ __forceinline__ void p0_prologue(const Frame& F) {
;     ...
;             for (int k = 0; k < 128; k += 8) {
;                 float w[8];
; #pragma unroll
;                 for (int q = 0; q < 8; ++q) w[q] = wm[(size_t)(k + q) * 6144];
; #pragma unroll
;                 for (int r = 0; r < 17; ++r) { const f32x4 s0 = *(LAS const f32x4*)(S + r * 1024 + 128 * wave + k), s1 = *(LAS const f32x4*)(S + r * 1024 + 128 * wave + k + 4);
;                     acc[r] += s0[0] * w[0] + s0[1] * w[1] + s0[2] * w[2] + s0[3] * w[3] + s1[0] * w[4] + s1[1] * w[5] + s1[2] * w[6] + s1[3] * w[7]; }
	v_mov_b32_e32 v145, v156
	v_mov_b32_e32 v156, v149
	v_mov_b32_e32 v42, v50
	v_mov_b32_e32 v43, v58
	v_mov_b32_e32 v58, v51
	v_mov_b32_e32 v50, v54
	v_mov_b32_e32 v51, v62
	v_mov_b32_e32 v62, v55
	v_mov_b32_e32 v54, v66
	v_mov_b32_e32 v55, v74
	v_mov_b32_e32 v74, v67
	v_mov_b32_e32 v66, v70
	v_mov_b32_e32 v67, v78
	v_mov_b32_e32 v78, v71
	v_mov_b32_e32 v70, v82
	v_mov_b32_e32 v71, v90
	v_pk_mul_f32 v[32:33], v[170:171], v[32:33] op_sel_hi:[0,1]
	v_pk_mul_f32 v[56:57], v[170:171], v[56:57] op_sel_hi:[0,1]
	v_pk_mul_f32 v[72:73], v[170:171], v[72:73] op_sel_hi:[0,1]
	v_pk_mul_f32 v[88:89], v[170:171], v[88:89] op_sel_hi:[0,1]
	v_pk_mul_f32 v[104:105], v[170:171], v[104:105] op_sel_hi:[0,1]
	v_pk_mul_f32 v[120:121], v[170:171], v[120:121] op_sel_hi:[0,1]
	v_pk_mul_f32 v[136:137], v[170:171], v[136:137] op_sel_hi:[0,1]
	v_pk_mul_f32 v[148:149], v[170:171], v[152:153] op_sel_hi:[0,1]
	v_mov_b32_e32 v90, v83
	v_mov_b32_e32 v82, v86
	v_mov_b32_e32 v83, v94
	v_mov_b32_e32 v94, v87
	v_mov_b32_e32 v86, v98
	v_mov_b32_e32 v87, v106
	v_mov_b32_e32 v106, v99
	v_mov_b32_e32 v98, v102
	v_mov_b32_e32 v99, v110
	v_mov_b32_e32 v110, v103
	v_mov_b32_e32 v102, v114
	v_mov_b32_e32 v103, v122
	v_mov_b32_e32 v122, v115
	v_mov_b32_e32 v114, v118
	v_mov_b32_e32 v115, v126
	v_mov_b32_e32 v126, v119
	v_mov_b32_e32 v118, v130
	v_mov_b32_e32 v119, v138
	v_mov_b32_e32 v138, v131
	v_mov_b32_e32 v130, v134
	v_mov_b32_e32 v131, v142
	v_mov_b32_e32 v142, v135
	v_mov_b32_e32 v134, v146
	v_mov_b32_e32 v135, v154
	v_pk_fma_f32 v[32:33], v[168:169], v[36:37], v[32:33] op_sel_hi:[0,1,1]
	v_pk_fma_f32 v[30:31], v[168:169], v[30:31], v[56:57] op_sel_hi:[0,1,1]
	v_pk_fma_f32 v[36:37], v[168:169], v[52:53], v[72:73] op_sel_hi:[0,1,1]
	v_pk_fma_f32 v[52:53], v[168:169], v[68:69], v[88:89] op_sel_hi:[0,1,1]
	v_pk_fma_f32 v[56:57], v[168:169], v[84:85], v[104:105] op_sel_hi:[0,1,1]
	v_pk_fma_f32 v[68:69], v[168:169], v[100:101], v[120:121] op_sel_hi:[0,1,1]
	v_pk_fma_f32 v[72:73], v[168:169], v[116:117], v[136:137] op_sel_hi:[0,1,1]
	v_pk_fma_f32 v[84:85], v[168:169], v[132:133], v[148:149] op_sel_hi:[0,1,1]
	v_mov_b32_e32 v169, v170
	v_mov_b32_e32 v154, v147
	v_pk_fma_f32 v[24:25], v[172:173], v[24:25], v[32:33] op_sel_hi:[0,1,1]
	v_pk_fma_f32 v[30:31], v[172:173], v[42:43], v[30:31] op_sel_hi:[0,1,1]
	v_pk_fma_f32 v[32:33], v[172:173], v[54:55], v[36:37] op_sel_hi:[0,1,1]
	v_pk_fma_f32 v[36:37], v[172:173], v[70:71], v[52:53] op_sel_hi:[0,1,1]
	v_pk_fma_f32 v[42:43], v[172:173], v[86:87], v[56:57] op_sel_hi:[0,1,1]
	v_pk_fma_f32 v[52:53], v[172:173], v[102:103], v[68:69] op_sel_hi:[0,1,1]
	v_pk_fma_f32 v[54:55], v[172:173], v[118:119], v[72:73] op_sel_hi:[0,1,1]
	v_pk_fma_f32 v[56:57], v[172:173], v[134:135], v[84:85] op_sel_hi:[0,1,1]
	s_waitcnt lgkmcnt(1)
	v_pk_mul_f32 v[68:69], v[168:169], v[160:161]
	v_mov_b32_e32 v173, v174
	v_pk_fma_f32 v[24:25], v[174:175], v[34:35], v[24:25] op_sel_hi:[0,1,1]
	v_pk_fma_f32 v[30:31], v[174:175], v[58:59], v[30:31] op_sel_hi:[0,1,1]
	v_pk_fma_f32 v[32:33], v[174:175], v[74:75], v[32:33] op_sel_hi:[0,1,1]
	v_pk_fma_f32 v[34:35], v[174:175], v[90:91], v[36:37] op_sel_hi:[0,1,1]
	v_pk_fma_f32 v[36:37], v[174:175], v[106:107], v[42:43] op_sel_hi:[0,1,1]
	v_pk_fma_f32 v[42:43], v[174:175], v[122:123], v[52:53] op_sel_hi:[0,1,1]
	v_pk_fma_f32 v[52:53], v[174:175], v[138:139], v[54:55] op_sel_hi:[0,1,1]
	v_pk_fma_f32 v[54:55], v[174:175], v[154:155], v[56:57] op_sel_hi:[0,1,1]
	v_pk_mul_f32 v[56:57], v[172:173], v[162:163]
	v_add_f32_e32 v58, v68, v69
	v_pk_fma_f32 v[24:25], v[176:177], v[26:27], v[24:25] op_sel_hi:[0,1,1]
	v_pk_fma_f32 v[26:27], v[176:177], v[48:49], v[30:31] op_sel_hi:[0,1,1]
	v_pk_fma_f32 v[30:31], v[176:177], v[64:65], v[32:33] op_sel_hi:[0,1,1]
	v_pk_fma_f32 v[32:33], v[176:177], v[80:81], v[34:35] op_sel_hi:[0,1,1]
	v_pk_fma_f32 v[34:35], v[176:177], v[96:97], v[36:37] op_sel_hi:[0,1,1]
	v_pk_fma_f32 v[36:37], v[176:177], v[112:113], v[42:43] op_sel_hi:[0,1,1]
	v_pk_fma_f32 v[42:43], v[176:177], v[128:129], v[52:53] op_sel_hi:[0,1,1]
	v_pk_fma_f32 v[48:49], v[176:177], v[144:145], v[54:55] op_sel_hi:[0,1,1]
	v_mov_b32_e32 v177, v178
	v_add_f32_e32 v52, v56, v58
	v_mov_b32_e32 v146, v150
	v_mov_b32_e32 v147, v158
	v_pk_fma_f32 v[24:25], v[178:179], v[44:45], v[24:25] op_sel_hi:[0,1,1]
	v_pk_fma_f32 v[26:27], v[178:179], v[60:61], v[26:27] op_sel_hi:[0,1,1]
	v_pk_fma_f32 v[30:31], v[178:179], v[76:77], v[30:31] op_sel_hi:[0,1,1]
	v_pk_fma_f32 v[32:33], v[178:179], v[92:93], v[32:33] op_sel_hi:[0,1,1]
	v_pk_fma_f32 v[34:35], v[178:179], v[108:109], v[34:35] op_sel_hi:[0,1,1]
	v_pk_fma_f32 v[36:37], v[178:179], v[124:125], v[36:37] op_sel_hi:[0,1,1]
	v_pk_fma_f32 v[42:43], v[178:179], v[140:141], v[42:43] op_sel_hi:[0,1,1]
	v_pk_fma_f32 v[44:45], v[178:179], v[156:157], v[48:49] op_sel_hi:[0,1,1]
	s_waitcnt lgkmcnt(0)
; #define LAS __attribute__((address_space(3)))
; __device__ __forceinline__ void p0_prologue(const Frame& F) {
;     ...
;             for (int k = 0; k < 128; k += 8) {
;                 float w[8];
; #pragma unroll
;                 for (int q = 0; q < 8; ++q) w[q] = wm[(size_t)(k + q) * 6144];
; #pragma unroll
;                 for (int r = 0; r < 17; ++r) { const f32x4 s0 = *(LAS const f32x4*)(S + r * 1024 + 128 * wave + k), s1 = *(LAS const f32x4*)(S + r * 1024 + 128 * wave + k + 4);
;                     acc[r] += s0[0] * w[0] + s0[1] * w[1] + s0[2] * w[2] + s0[3] * w[3] + s1[0] * w[4] + s1[1] * w[5] + s1[2] * w[6] + s1[3] * w[7]; }
	v_pk_mul_f32 v[48:49], v[176:177], v[164:165]
	v_add_f32_e32 v52, v57, v52
	v_mov_b32_e32 v158, v151
	v_pk_fma_f32 v[24:25], v[180:181], v[28:29], v[24:25] op_sel_hi:[0,1,1]
	v_pk_fma_f32 v[26:27], v[180:181], v[50:51], v[26:27] op_sel_hi:[0,1,1]
	v_pk_fma_f32 v[28:29], v[180:181], v[66:67], v[30:31] op_sel_hi:[0,1,1]
	v_pk_fma_f32 v[30:31], v[180:181], v[82:83], v[32:33] op_sel_hi:[0,1,1]
	v_pk_fma_f32 v[32:33], v[180:181], v[98:99], v[34:35] op_sel_hi:[0,1,1]
	v_pk_fma_f32 v[34:35], v[180:181], v[114:115], v[36:37] op_sel_hi:[0,1,1]
	v_pk_fma_f32 v[36:37], v[180:181], v[130:131], v[42:43] op_sel_hi:[0,1,1]
	v_pk_fma_f32 v[42:43], v[180:181], v[146:147], v[44:45] op_sel_hi:[0,1,1]
	v_mov_b32_e32 v181, v2
	v_add_f32_e32 v48, v48, v52
	v_pk_fma_f32 v[24:25], v[2:3], v[46:47], v[24:25] op_sel_hi:[0,1,1]
	v_pk_fma_f32 v[26:27], v[2:3], v[62:63], v[26:27] op_sel_hi:[0,1,1]
	v_pk_fma_f32 v[28:29], v[2:3], v[78:79], v[28:29] op_sel_hi:[0,1,1]
	v_pk_fma_f32 v[30:31], v[2:3], v[94:95], v[30:31] op_sel_hi:[0,1,1]
	v_pk_fma_f32 v[32:33], v[2:3], v[110:111], v[32:33] op_sel_hi:[0,1,1]
	v_pk_fma_f32 v[34:35], v[2:3], v[126:127], v[34:35] op_sel_hi:[0,1,1]
	v_pk_fma_f32 v[36:37], v[2:3], v[142:143], v[36:37] op_sel_hi:[0,1,1]
	v_pk_fma_f32 v[42:43], v[2:3], v[158:159], v[42:43] op_sel_hi:[0,1,1]
	v_pk_mul_f32 v[44:45], v[180:181], v[166:167]
	v_add_f32_e32 v2, v49, v48
	v_add_f32_e32 v2, v44, v2
	s_add_i32 s11, s11, 32
	v_add_f32_e32 v2, v45, v2
	v_pk_add_f32 v[8:9], v[8:9], v[24:25]
	v_pk_add_f32 v[10:11], v[10:11], v[26:27]
	v_pk_add_f32 v[12:13], v[12:13], v[28:29]
	v_pk_add_f32 v[14:15], v[14:15], v[30:31]
	v_pk_add_f32 v[16:17], v[16:17], v[32:33]
	v_pk_add_f32 v[18:19], v[18:19], v[34:35]
	v_pk_add_f32 v[20:21], v[20:21], v[36:37]
	v_pk_add_f32 v[22:23], v[22:23], v[42:43]
	v_add_f32_e32 v41, v41, v2
	s_waitcnt vmcnt(0)
	v_mov_b32_e32 v2, v206
	v_mov_b32_e32 v168, v207
	v_mov_b32_e32 v170, v208
	v_mov_b32_e32 v172, v209
	v_mov_b32_e32 v174, v210
	v_mov_b32_e32 v176, v211
	v_mov_b32_e32 v178, v212
	v_mov_b32_e32 v180, v213
	v_mov_b32_e32 v42, s11
	s_add_i32 s10, s10, 8
	ds_read_b128 v[24:27], v42
	ds_read_b128 v[28:31], v42 offset:16
	ds_read_b128 v[32:35], v42 offset:4096
	ds_read_b128 v[44:47], v42 offset:4112
	ds_read_b128 v[48:51], v42 offset:8192
	ds_read_b128 v[52:55], v42 offset:8208
	ds_read_b128 v[56:59], v42 offset:12288
	ds_read_b128 v[60:63], v42 offset:12304
	ds_read_b128 v[64:67], v42 offset:16384
	ds_read_b128 v[68:71], v42 offset:16400
	ds_read_b128 v[72:75], v42 offset:20480
	ds_read_b128 v[76:79], v42 offset:20496
	ds_read_b128 v[80:83], v42 offset:24576
	ds_read_b128 v[84:87], v42 offset:24592
	ds_read_b128 v[88:91], v42 offset:28672
	ds_read_b128 v[92:95], v42 offset:28688
	ds_read_b128 v[96:99], v42 offset:32768
	ds_read_b128 v[100:103], v42 offset:32784
	ds_read_b128 v[104:107], v42 offset:36864
	ds_read_b128 v[108:111], v42 offset:36880
	ds_read_b128 v[112:115], v42 offset:40960
	ds_read_b128 v[116:119], v42 offset:40976
	ds_read_b128 v[120:123], v42 offset:45056
	ds_read_b128 v[124:127], v42 offset:45072
	ds_read_b128 v[128:131], v42 offset:49152
	ds_read_b128 v[132:135], v42 offset:49168
	ds_read_b128 v[136:139], v42 offset:53248
	ds_read_b128 v[140:143], v42 offset:53264
	ds_read_b128 v[144:147], v42 offset:57344
	ds_read_b128 v[148:151], v42 offset:57360
	ds_read_b128 v[152:155], v42 offset:61440
	ds_read_b128 v[156:159], v42 offset:61456
	s_add_i32 s4, s11, 0x10000
	s_add_i32 s5, s11, 0x10010
	v_mov_b32_e32 v36, s4
	v_mov_b32_e32 v37, s5
	ds_read_b128 v[160:163], v36
	ds_read_b128 v[164:167], v37
	s_waitcnt lgkmcnt(14)
	v_mov_b32_e32 v37, v32
	v_mov_b32_e32 v32, v25
	v_mov_b32_e32 v25, v34
	v_mov_b32_e32 v34, v27
	v_mov_b32_e32 v27, v44
	v_mov_b32_e32 v44, v29
	v_mov_b32_e32 v29, v46
	v_mov_b32_e32 v46, v31
	v_mov_b32_e32 v31, v56
	v_mov_b32_e32 v56, v49
	v_mov_b32_e32 v49, v60
	v_mov_b32_e32 v60, v53
	v_mov_b32_e32 v53, v72
	v_mov_b32_e32 v72, v65
	v_mov_b32_e32 v65, v76
	v_mov_b32_e32 v76, v69
	v_mov_b32_e32 v69, v88
	v_mov_b32_e32 v88, v81
	v_mov_b32_e32 v81, v92
	v_mov_b32_e32 v92, v85
	v_mov_b32_e32 v85, v104
	v_mov_b32_e32 v104, v97
	v_mov_b32_e32 v97, v108
	v_mov_b32_e32 v108, v101
	s_waitcnt lgkmcnt(11)
	v_mov_b32_e32 v101, v120
	v_mov_b32_e32 v120, v113
	s_waitcnt lgkmcnt(10)
	v_mov_b32_e32 v113, v124
	v_mov_b32_e32 v124, v117
	s_waitcnt lgkmcnt(7)
	v_mov_b32_e32 v117, v136
	v_mov_b32_e32 v136, v129
	s_waitcnt lgkmcnt(6)
	v_mov_b32_e32 v129, v140
	v_mov_b32_e32 v140, v133
	s_waitcnt lgkmcnt(3)
	v_mov_b32_e32 v133, v152
	v_mov_b32_e32 v152, v145
	v_mov_b32_e32 v36, v24
	v_mov_b32_e32 v24, v26
	v_mov_b32_e32 v26, v28
	v_mov_b32_e32 v28, v30
	v_mov_b32_e32 v30, v48
	v_mov_b32_e32 v48, v52
	v_mov_b32_e32 v52, v64
	v_mov_b32_e32 v64, v68
	v_mov_b32_e32 v68, v80
	v_mov_b32_e32 v80, v84
	v_mov_b32_e32 v84, v96
	v_mov_b32_e32 v96, v100
	v_mov_b32_e32 v100, v112
	v_mov_b32_e32 v112, v116
	v_mov_b32_e32 v116, v128
	v_mov_b32_e32 v128, v132
	v_mov_b32_e32 v132, v144
	v_mov_b32_e32 v144, v148
	s_waitcnt lgkmcnt(2)
; #define LAS __attribute__((address_space(3)))
; __device__ __forceinline__ void p0_prologue(const Frame& F) {
;     ...
;             for (int k = 0; k < 128; k += 8) {
;                 float w[8];
; #pragma unroll
;                 for (int q = 0; q < 8; ++q) w[q] = wm[(size_t)(k + q) * 6144];
; #pragma unroll
;                 for (int r = 0; r < 17; ++r) { const f32x4 s0 = *(LAS const f32x4*)(S + r * 1024 + 128 * wave + k), s1 = *(LAS const f32x4*)(S + r * 1024 + 128 * wave + k + 4);
;                     acc[r] += s0[0] * w[0] + s0[1] * w[1] + s0[2] * w[2] + s0[3] * w[3] + s1[0] * w[4] + s1[1] * w[5] + s1[2] * w[6] + s1[3] * w[7]; }
	v_mov_b32_e32 v145, v156
	v_mov_b32_e32 v156, v149
	v_mov_b32_e32 v42, v50
	v_mov_b32_e32 v43, v58
	v_mov_b32_e32 v58, v51
	v_mov_b32_e32 v50, v54
	v_mov_b32_e32 v51, v62
	v_mov_b32_e32 v62, v55
	v_mov_b32_e32 v54, v66
	v_mov_b32_e32 v55, v74
	v_mov_b32_e32 v74, v67
	v_mov_b32_e32 v66, v70
	v_mov_b32_e32 v67, v78
	v_mov_b32_e32 v78, v71
	v_mov_b32_e32 v70, v82
	v_mov_b32_e32 v71, v90
	v_pk_mul_f32 v[32:33], v[170:171], v[32:33] op_sel_hi:[0,1]
	v_pk_mul_f32 v[56:57], v[170:171], v[56:57] op_sel_hi:[0,1]
	v_pk_mul_f32 v[72:73], v[170:171], v[72:73] op_sel_hi:[0,1]
	v_pk_mul_f32 v[88:89], v[170:171], v[88:89] op_sel_hi:[0,1]
	v_pk_mul_f32 v[104:105], v[170:171], v[104:105] op_sel_hi:[0,1]
	v_pk_mul_f32 v[120:121], v[170:171], v[120:121] op_sel_hi:[0,1]
	v_pk_mul_f32 v[136:137], v[170:171], v[136:137] op_sel_hi:[0,1]
	v_pk_mul_f32 v[148:149], v[170:171], v[152:153] op_sel_hi:[0,1]
	v_mov_b32_e32 v90, v83
	v_mov_b32_e32 v82, v86
	v_mov_b32_e32 v83, v94
	v_mov_b32_e32 v94, v87
	v_mov_b32_e32 v86, v98
	v_mov_b32_e32 v87, v106
	v_mov_b32_e32 v106, v99
	v_mov_b32_e32 v98, v102
	v_mov_b32_e32 v99, v110
	v_mov_b32_e32 v110, v103
	v_mov_b32_e32 v102, v114
	v_mov_b32_e32 v103, v122
	v_mov_b32_e32 v122, v115
	v_mov_b32_e32 v114, v118
	v_mov_b32_e32 v115, v126
	v_mov_b32_e32 v126, v119
	v_mov_b32_e32 v118, v130
	v_mov_b32_e32 v119, v138
	v_mov_b32_e32 v138, v131
	v_mov_b32_e32 v130, v134
	v_mov_b32_e32 v131, v142
	v_mov_b32_e32 v142, v135
	v_mov_b32_e32 v134, v146
	v_mov_b32_e32 v135, v154
	v_pk_fma_f32 v[32:33], v[168:169], v[36:37], v[32:33] op_sel_hi:[0,1,1]
	v_pk_fma_f32 v[30:31], v[168:169], v[30:31], v[56:57] op_sel_hi:[0,1,1]
	v_pk_fma_f32 v[36:37], v[168:169], v[52:53], v[72:73] op_sel_hi:[0,1,1]
	v_pk_fma_f32 v[52:53], v[168:169], v[68:69], v[88:89] op_sel_hi:[0,1,1]
	v_pk_fma_f32 v[56:57], v[168:169], v[84:85], v[104:105] op_sel_hi:[0,1,1]
	v_pk_fma_f32 v[68:69], v[168:169], v[100:101], v[120:121] op_sel_hi:[0,1,1]
	v_pk_fma_f32 v[72:73], v[168:169], v[116:117], v[136:137] op_sel_hi:[0,1,1]
	v_pk_fma_f32 v[84:85], v[168:169], v[132:133], v[148:149] op_sel_hi:[0,1,1]
	v_mov_b32_e32 v169, v170
	v_mov_b32_e32 v154, v147
	v_pk_fma_f32 v[24:25], v[172:173], v[24:25], v[32:33] op_sel_hi:[0,1,1]
	v_pk_fma_f32 v[30:31], v[172:173], v[42:43], v[30:31] op_sel_hi:[0,1,1]
	v_pk_fma_f32 v[32:33], v[172:173], v[54:55], v[36:37] op_sel_hi:[0,1,1]
	v_pk_fma_f32 v[36:37], v[172:173], v[70:71], v[52:53] op_sel_hi:[0,1,1]
	v_pk_fma_f32 v[42:43], v[172:173], v[86:87], v[56:57] op_sel_hi:[0,1,1]
	v_pk_fma_f32 v[52:53], v[172:173], v[102:103], v[68:69] op_sel_hi:[0,1,1]
	v_pk_fma_f32 v[54:55], v[172:173], v[118:119], v[72:73] op_sel_hi:[0,1,1]
	v_pk_fma_f32 v[56:57], v[172:173], v[134:135], v[84:85] op_sel_hi:[0,1,1]
	s_waitcnt lgkmcnt(1)
; #define LAS __attribute__((address_space(3)))
; __device__ __forceinline__ void p0_prologue(const Frame& F) {
;     ...
;             for (int k = 0; k < 128; k += 8) {
;                 float w[8];
; #pragma unroll
;                 for (int q = 0; q < 8; ++q) w[q] = wm[(size_t)(k + q) * 6144];
; #pragma unroll
;                 for (int r = 0; r < 17; ++r) { const f32x4 s0 = *(LAS const f32x4*)(S + r * 1024 + 128 * wave + k), s1 = *(LAS const f32x4*)(S + r * 1024 + 128 * wave + k + 4);
;                     acc[r] += s0[0] * w[0] + s0[1] * w[1] + s0[2] * w[2] + s0[3] * w[3] + s1[0] * w[4] + s1[1] * w[5] + s1[2] * w[6] + s1[3] * w[7]; }
;             }
; #pragma unroll
;             for (int r = 0; r < 17; ++r) red[(wave * 17 + r) * 64 + lane] = acc[r];
;             __syncthreads();
;             for (int o = F.tid; o < 17 * 64; o += NTHREADS) { const int r = o >> 6, cc = o & 63; float a = 0.f;
; #pragma unroll
;                 for (int w = 0; w < 8; ++w) a += red[(w * 17 + r) * 64 + cc];
;                 modp[((size_t)l * 17 + r) * 6144 + cb * 64 + cc] = a + bmod[l * 6144 + cb * 64 + cc]; }
	v_pk_mul_f32 v[68:69], v[168:169], v[160:161]
	v_mov_b32_e32 v173, v174
	v_pk_fma_f32 v[24:25], v[174:175], v[34:35], v[24:25] op_sel_hi:[0,1,1]
	v_pk_fma_f32 v[30:31], v[174:175], v[58:59], v[30:31] op_sel_hi:[0,1,1]
	v_pk_fma_f32 v[32:33], v[174:175], v[74:75], v[32:33] op_sel_hi:[0,1,1]
	v_pk_fma_f32 v[34:35], v[174:175], v[90:91], v[36:37] op_sel_hi:[0,1,1]
	v_pk_fma_f32 v[36:37], v[174:175], v[106:107], v[42:43] op_sel_hi:[0,1,1]
	v_pk_fma_f32 v[42:43], v[174:175], v[122:123], v[52:53] op_sel_hi:[0,1,1]
	v_pk_fma_f32 v[52:53], v[174:175], v[138:139], v[54:55] op_sel_hi:[0,1,1]
	v_pk_fma_f32 v[54:55], v[174:175], v[154:155], v[56:57] op_sel_hi:[0,1,1]
	v_pk_mul_f32 v[56:57], v[172:173], v[162:163]
	v_add_f32_e32 v58, v68, v69
	v_pk_fma_f32 v[24:25], v[176:177], v[26:27], v[24:25] op_sel_hi:[0,1,1]
	v_pk_fma_f32 v[26:27], v[176:177], v[48:49], v[30:31] op_sel_hi:[0,1,1]
	v_pk_fma_f32 v[30:31], v[176:177], v[64:65], v[32:33] op_sel_hi:[0,1,1]
	v_pk_fma_f32 v[32:33], v[176:177], v[80:81], v[34:35] op_sel_hi:[0,1,1]
	v_pk_fma_f32 v[34:35], v[176:177], v[96:97], v[36:37] op_sel_hi:[0,1,1]
	v_pk_fma_f32 v[36:37], v[176:177], v[112:113], v[42:43] op_sel_hi:[0,1,1]
	v_pk_fma_f32 v[42:43], v[176:177], v[128:129], v[52:53] op_sel_hi:[0,1,1]
	v_pk_fma_f32 v[48:49], v[176:177], v[144:145], v[54:55] op_sel_hi:[0,1,1]
	v_mov_b32_e32 v177, v178
	v_add_f32_e32 v52, v56, v58
	v_mov_b32_e32 v146, v150
	v_mov_b32_e32 v147, v158
	v_pk_fma_f32 v[24:25], v[178:179], v[44:45], v[24:25] op_sel_hi:[0,1,1]
	v_pk_fma_f32 v[26:27], v[178:179], v[60:61], v[26:27] op_sel_hi:[0,1,1]
	v_pk_fma_f32 v[30:31], v[178:179], v[76:77], v[30:31] op_sel_hi:[0,1,1]
	v_pk_fma_f32 v[32:33], v[178:179], v[92:93], v[32:33] op_sel_hi:[0,1,1]
	v_pk_fma_f32 v[34:35], v[178:179], v[108:109], v[34:35] op_sel_hi:[0,1,1]
	v_pk_fma_f32 v[36:37], v[178:179], v[124:125], v[36:37] op_sel_hi:[0,1,1]
	v_pk_fma_f32 v[42:43], v[178:179], v[140:141], v[42:43] op_sel_hi:[0,1,1]
	v_pk_fma_f32 v[44:45], v[178:179], v[156:157], v[48:49] op_sel_hi:[0,1,1]
	s_waitcnt lgkmcnt(0)
	v_pk_mul_f32 v[48:49], v[176:177], v[164:165]
	v_add_f32_e32 v52, v57, v52
	v_mov_b32_e32 v158, v151
	v_pk_fma_f32 v[24:25], v[180:181], v[28:29], v[24:25] op_sel_hi:[0,1,1]
	v_pk_fma_f32 v[26:27], v[180:181], v[50:51], v[26:27] op_sel_hi:[0,1,1]
	v_pk_fma_f32 v[28:29], v[180:181], v[66:67], v[30:31] op_sel_hi:[0,1,1]
	v_pk_fma_f32 v[30:31], v[180:181], v[82:83], v[32:33] op_sel_hi:[0,1,1]
	v_pk_fma_f32 v[32:33], v[180:181], v[98:99], v[34:35] op_sel_hi:[0,1,1]
	v_pk_fma_f32 v[34:35], v[180:181], v[114:115], v[36:37] op_sel_hi:[0,1,1]
	v_pk_fma_f32 v[36:37], v[180:181], v[130:131], v[42:43] op_sel_hi:[0,1,1]
	v_pk_fma_f32 v[42:43], v[180:181], v[146:147], v[44:45] op_sel_hi:[0,1,1]
	v_mov_b32_e32 v181, v2
	v_add_f32_e32 v48, v48, v52
	v_pk_fma_f32 v[24:25], v[2:3], v[46:47], v[24:25] op_sel_hi:[0,1,1]
	v_pk_fma_f32 v[26:27], v[2:3], v[62:63], v[26:27] op_sel_hi:[0,1,1]
	v_pk_fma_f32 v[28:29], v[2:3], v[78:79], v[28:29] op_sel_hi:[0,1,1]
	v_pk_fma_f32 v[30:31], v[2:3], v[94:95], v[30:31] op_sel_hi:[0,1,1]
	v_pk_fma_f32 v[32:33], v[2:3], v[110:111], v[32:33] op_sel_hi:[0,1,1]
	v_pk_fma_f32 v[34:35], v[2:3], v[126:127], v[34:35] op_sel_hi:[0,1,1]
	v_pk_fma_f32 v[36:37], v[2:3], v[142:143], v[36:37] op_sel_hi:[0,1,1]
	v_pk_fma_f32 v[42:43], v[2:3], v[158:159], v[42:43] op_sel_hi:[0,1,1]
	v_pk_mul_f32 v[44:45], v[180:181], v[166:167]
	v_add_f32_e32 v2, v49, v48
	v_add_f32_e32 v2, v44, v2
	s_add_i32 s11, s11, 32
	v_add_f32_e32 v2, v45, v2
	v_pk_add_f32 v[8:9], v[8:9], v[24:25]
	v_pk_add_f32 v[10:11], v[10:11], v[26:27]
	v_pk_add_f32 v[12:13], v[12:13], v[28:29]
	v_pk_add_f32 v[14:15], v[14:15], v[30:31]
	v_pk_add_f32 v[16:17], v[16:17], v[32:33]
	v_pk_add_f32 v[18:19], v[18:19], v[34:35]
	v_pk_add_f32 v[20:21], v[20:21], v[36:37]
	v_pk_add_f32 v[22:23], v[22:23], v[42:43]
	v_add_f32_e32 v41, v41, v2
	ds_write2st64_b32 v40, v8, v9 offset1:1
	ds_write2st64_b32 v40, v10, v11 offset0:2 offset1:3
	ds_write2st64_b32 v40, v12, v13 offset0:4 offset1:5
	ds_write2st64_b32 v40, v14, v15 offset0:6 offset1:7
	ds_write2st64_b32 v40, v16, v17 offset0:8 offset1:9
	ds_write2st64_b32 v40, v18, v19 offset0:10 offset1:11
	ds_write2st64_b32 v40, v20, v21 offset0:12 offset1:13
	ds_write2st64_b32 v40, v22, v23 offset0:14 offset1:15
	ds_write_b32 v40, v41 offset:4096
	s_waitcnt lgkmcnt(0)
	s_barrier
	s_and_saveexec_b64 s[10:11], vcc
	s_cbranch_execz .LBB0_11
	s_mul_i32 s4, s9, 0x1800
	s_add_i32 s4, s4, s8
	v_or_b32_e32 v6, s4, v1
	s_mul_hi_i32 s13, s9, 17
	s_mul_i32 s12, s9, 17
	s_ashr_i32 s9, s8, 31
	v_ashrrev_i32_e32 v7, 31, v6
	v_lshl_add_u64 v[6:7], v[6:7], 2, s[2:3]
	v_lshl_add_u64 v[8:9], s[8:9], 2, v[4:5]
	s_mov_b64 s[8:9], 0
	v_mov_b32_e32 v2, v0
